# baseline (speedup 1.0000x reference)
.LBB3_8:
	s_waitcnt vmcnt(30)
	v_cvt_f32_i32_sdwa v69, sext(v66) dst_sel:DWORD dst_unused:UNUSED_PAD src0_sel:WORD_0
	v_cvt_f32_i32_sdwa v68, sext(v62) dst_sel:DWORD dst_unused:UNUSED_PAD src0_sel:WORD_0
	v_cvt_f32_i32_sdwa v87, sext(v66) dst_sel:DWORD dst_unused:UNUSED_PAD src0_sel:WORD_1
	v_cvt_f32_i32_sdwa v86, sext(v62) dst_sel:DWORD dst_unused:UNUSED_PAD src0_sel:WORD_1
	v_cvt_f32_i32_sdwa v88, sext(v63) dst_sel:DWORD dst_unused:UNUSED_PAD src0_sel:WORD_1
	v_cvt_f32_i32_sdwa v66, sext(v63) dst_sel:DWORD dst_unused:UNUSED_PAD src0_sel:WORD_0
	s_waitcnt vmcnt(28)
	v_cvt_f32_i32_sdwa v63, sext(v58) dst_sel:DWORD dst_unused:UNUSED_PAD src0_sel:WORD_0
	v_cvt_f32_i32_sdwa v62, sext(v54) dst_sel:DWORD dst_unused:UNUSED_PAD src0_sel:WORD_0
	v_cvt_f32_i32_sdwa v91, sext(v58) dst_sel:DWORD dst_unused:UNUSED_PAD src0_sel:WORD_1
	v_cvt_f32_i32_sdwa v90, sext(v54) dst_sel:DWORD dst_unused:UNUSED_PAD src0_sel:WORD_1
	s_waitcnt lgkmcnt(0)
	s_mov_b32 s88, s20
	v_cvt_f32_i32_sdwa v92, sext(v55) dst_sel:DWORD dst_unused:UNUSED_PAD src0_sel:WORD_1
	v_cvt_f32_i32_sdwa v58, sext(v55) dst_sel:DWORD dst_unused:UNUSED_PAD src0_sel:WORD_0
	s_waitcnt vmcnt(26)
	v_cvt_f32_i32_sdwa v55, sext(v64) dst_sel:DWORD dst_unused:UNUSED_PAD src0_sel:WORD_0
	v_cvt_f32_i32_sdwa v54, sext(v60) dst_sel:DWORD dst_unused:UNUSED_PAD src0_sel:WORD_0
	v_cvt_f32_i32_sdwa v95, sext(v64) dst_sel:DWORD dst_unused:UNUSED_PAD src0_sel:WORD_1
	v_cvt_f32_i32_sdwa v94, sext(v60) dst_sel:DWORD dst_unused:UNUSED_PAD src0_sel:WORD_1
	v_cvt_f32_i32_sdwa v96, sext(v61) dst_sel:DWORD dst_unused:UNUSED_PAD src0_sel:WORD_1
	v_cvt_f32_i32_sdwa v64, sext(v61) dst_sel:DWORD dst_unused:UNUSED_PAD src0_sel:WORD_0
	s_waitcnt vmcnt(24)
	v_cvt_f32_i32_sdwa v61, sext(v56) dst_sel:DWORD dst_unused:UNUSED_PAD src0_sel:WORD_0
	v_cvt_f32_i32_sdwa v60, sext(v52) dst_sel:DWORD dst_unused:UNUSED_PAD src0_sel:WORD_0
	v_cvt_f32_i32_sdwa v99, sext(v56) dst_sel:DWORD dst_unused:UNUSED_PAD src0_sel:WORD_1
	v_cvt_f32_i32_sdwa v98, sext(v52) dst_sel:DWORD dst_unused:UNUSED_PAD src0_sel:WORD_1
	v_cvt_f32_i32_sdwa v100, sext(v53) dst_sel:DWORD dst_unused:UNUSED_PAD src0_sel:WORD_1
	v_cvt_f32_i32_sdwa v56, sext(v53) dst_sel:DWORD dst_unused:UNUSED_PAD src0_sel:WORD_0
	v_pk_mul_f32 v[52:53], s[88:89], v[68:69]
	v_pk_mul_f32 v[68:69], s[88:89], v[86:87]
	v_mov_b32_e32 v87, v52
	v_mov_b32_e32 v86, v68
	v_mov_b32_e32 v52, v69
	v_pk_add_f32 v[68:69], v[86:87], 0 op_sel_hi:[1,0]
	v_pk_mul_f32 v[62:63], s[86:87], v[62:63]
	v_pk_add_f32 v[52:53], v[68:69], v[52:53]
	v_pk_mul_f32 v[68:69], s[86:87], v[90:91]
	v_mov_b32_e32 v87, v62
	v_mov_b32_e32 v86, v68
	v_pk_add_f32 v[52:53], v[52:53], v[86:87]
	v_mov_b32_e32 v62, v69
	v_pk_add_f32 v[52:53], v[52:53], v[62:63]
	v_pk_mul_f32 v[54:55], s[82:83], v[54:55]
	v_pk_mul_f32 v[62:63], s[82:83], v[94:95]
	v_mov_b32_e32 v69, v54
	v_mov_b32_e32 v68, v62
	v_cvt_f32_i32_sdwa v89, sext(v67) dst_sel:DWORD dst_unused:UNUSED_PAD src0_sel:WORD_1
	v_cvt_f32_i32_sdwa v67, sext(v67) dst_sel:DWORD dst_unused:UNUSED_PAD src0_sel:WORD_0
	v_pk_add_f32 v[52:53], v[52:53], v[68:69]
	v_mov_b32_e32 v54, v63
	v_cvt_f32_i32_sdwa v93, sext(v59) dst_sel:DWORD dst_unused:UNUSED_PAD src0_sel:WORD_1
	v_cvt_f32_i32_sdwa v59, sext(v59) dst_sel:DWORD dst_unused:UNUSED_PAD src0_sel:WORD_0
	v_pk_add_f32 v[52:53], v[52:53], v[54:55]
	v_pk_mul_f32 v[54:55], s[84:85], v[60:61]
	v_pk_mul_f32 v[60:61], s[84:85], v[98:99]
	v_mov_b32_e32 v63, v54
	v_mov_b32_e32 v62, v60
	v_pk_add_f32 v[52:53], v[52:53], v[62:63]
	v_mov_b32_e32 v54, v61
	v_pk_add_f32 v[52:53], v[52:53], v[54:55]
	v_pk_mul_f32 v[54:55], s[88:89], v[88:89]
	v_pk_mul_f32 v[60:61], s[88:89], v[66:67]
	v_mov_b32_e32 v62, v54
	v_mov_b32_e32 v63, v60
	v_pk_mul_f32 v[58:59], s[86:87], v[58:59]
	v_mov_b32_e32 v60, v55
	v_pk_add_f32 v[54:55], v[62:63], 0 op_sel_hi:[1,0]
	v_mov_b32_e32 v63, v58
	v_add_f32_e64 v58, s24, 0
	v_add_f32_e32 v58, s99, v58
	v_add_f32_e32 v58, s3, v58
	v_add_f32_e32 v58, s16, v58
	v_add_f32_e32 v58, s33, v58
	v_add_f32_e32 v58, s17, v58
	v_pk_add_f32 v[54:55], v[54:55], v[60:61]
	v_pk_mul_f32 v[60:61], s[86:87], v[92:93]
	v_add_f32_e32 v58, s18, v58
	v_mov_b32_e32 v62, v60
	v_add_f32_e32 v60, s19, v58
	v_cvt_f32_i32_sdwa v97, sext(v65) dst_sel:DWORD dst_unused:UNUSED_PAD src0_sel:WORD_1
	v_cvt_f32_i32_sdwa v65, sext(v65) dst_sel:DWORD dst_unused:UNUSED_PAD src0_sel:WORD_0
	v_rcp_f32_e32 v60, v60
	v_cvt_f32_i32_sdwa v101, sext(v57) dst_sel:DWORD dst_unused:UNUSED_PAD src0_sel:WORD_1
	v_cvt_f32_i32_sdwa v57, sext(v57) dst_sel:DWORD dst_unused:UNUSED_PAD src0_sel:WORD_0
	v_pk_add_f32 v[54:55], v[54:55], v[62:63]
	v_pk_mul_f32 v[62:63], s[82:83], v[96:97]
	v_mov_b32_e32 v58, v61
	v_pk_mul_f32 v[64:65], s[82:83], v[64:65]
	v_pk_mul_f32 v[52:53], v[60:61], v[52:53] op_sel_hi:[0,1]
	v_mul_f32_e32 v61, 0x3fb8aa3b, v53
	v_pk_add_f32 v[54:55], v[54:55], v[58:59]
	v_mov_b32_e32 v58, v62
	v_mov_b32_e32 v59, v64
	v_pk_mul_f32 v[66:67], s[84:85], v[100:101]
	v_pk_mul_f32 v[56:57], s[84:85], v[56:57]
	v_exp_f32_e32 v61, v61
	v_pk_add_f32 v[58:59], v[54:55], v[58:59]
	v_mul_f32_e32 v54, 0x3fb8aa3b, v52
	v_mov_b32_e32 v64, v63
	v_exp_f32_e32 v54, v54
	v_pk_add_f32 v[58:59], v[58:59], v[64:65]
	v_mov_b32_e32 v62, v66
	v_mov_b32_e32 v63, v56
	v_pk_add_f32 v[58:59], v[58:59], v[62:63]
	v_mov_b32_e32 v56, v67
	v_pk_add_f32 v[56:57], v[58:59], v[56:57]
	v_add_f32_e32 v55, -1.0, v61
	v_cmp_lt_f32_e32 vcc, 0, v53
	v_pk_mul_f32 v[56:57], v[60:61], v[56:57] op_sel_hi:[0,1]
	s_waitcnt vmcnt(22)
	v_cvt_f32_i32_sdwa v59, sext(v50) dst_sel:DWORD dst_unused:UNUSED_PAD src0_sel:WORD_0
	v_cndmask_b32_e32 v55, v55, v53, vcc
	v_add_f32_e32 v53, -1.0, v54
	v_mul_f32_e32 v54, 0x3fb8aa3b, v57
	v_cmp_lt_f32_e32 vcc, 0, v52
	v_cvt_f32_i32_sdwa v58, sext(v48) dst_sel:DWORD dst_unused:UNUSED_PAD src0_sel:WORD_0
	v_cvt_f32_i32_sdwa v61, sext(v50) dst_sel:DWORD dst_unused:UNUSED_PAD src0_sel:WORD_1
	v_cvt_f32_i32_sdwa v60, sext(v48) dst_sel:DWORD dst_unused:UNUSED_PAD src0_sel:WORD_1
	v_exp_f32_e32 v54, v54
	v_cndmask_b32_e32 v52, v53, v52, vcc
	v_mul_f32_e32 v53, 0x3fb8aa3b, v56
	v_exp_f32_e32 v53, v53
	s_mov_b32 s20, s21
	s_mov_b32 s21, s50
	v_cvt_f32_i32_sdwa v62, sext(v49) dst_sel:DWORD dst_unused:UNUSED_PAD src0_sel:WORD_1
	v_cvt_f32_i32_sdwa v50, sext(v49) dst_sel:DWORD dst_unused:UNUSED_PAD src0_sel:WORD_0
	s_waitcnt vmcnt(20)
	v_cvt_f32_i32_sdwa v49, sext(v42) dst_sel:DWORD dst_unused:UNUSED_PAD src0_sel:WORD_0
	v_cvt_f32_i32_sdwa v48, sext(v40) dst_sel:DWORD dst_unused:UNUSED_PAD src0_sel:WORD_0
	v_cvt_f32_i32_sdwa v65, sext(v42) dst_sel:DWORD dst_unused:UNUSED_PAD src0_sel:WORD_1
	v_cvt_f32_i32_sdwa v64, sext(v40) dst_sel:DWORD dst_unused:UNUSED_PAD src0_sel:WORD_1
	v_cvt_f32_i32_sdwa v66, sext(v41) dst_sel:DWORD dst_unused:UNUSED_PAD src0_sel:WORD_1
	v_cvt_f32_i32_sdwa v42, sext(v41) dst_sel:DWORD dst_unused:UNUSED_PAD src0_sel:WORD_0
	s_waitcnt vmcnt(18)
	v_cvt_f32_i32_sdwa v41, sext(v46) dst_sel:DWORD dst_unused:UNUSED_PAD src0_sel:WORD_0
	v_cvt_f32_i32_sdwa v40, sext(v44) dst_sel:DWORD dst_unused:UNUSED_PAD src0_sel:WORD_0
	v_cvt_f32_i32_sdwa v69, sext(v46) dst_sel:DWORD dst_unused:UNUSED_PAD src0_sel:WORD_1
	v_cvt_f32_i32_sdwa v68, sext(v44) dst_sel:DWORD dst_unused:UNUSED_PAD src0_sel:WORD_1
	v_cvt_f32_i32_sdwa v86, sext(v45) dst_sel:DWORD dst_unused:UNUSED_PAD src0_sel:WORD_1
	v_cvt_f32_i32_sdwa v46, sext(v45) dst_sel:DWORD dst_unused:UNUSED_PAD src0_sel:WORD_0
	s_waitcnt vmcnt(16)
	v_cvt_f32_i32_sdwa v45, sext(v38) dst_sel:DWORD dst_unused:UNUSED_PAD src0_sel:WORD_0
	v_cvt_f32_i32_sdwa v44, sext(v36) dst_sel:DWORD dst_unused:UNUSED_PAD src0_sel:WORD_0
	v_cvt_f32_i32_sdwa v89, sext(v38) dst_sel:DWORD dst_unused:UNUSED_PAD src0_sel:WORD_1
	v_cvt_f32_i32_sdwa v88, sext(v36) dst_sel:DWORD dst_unused:UNUSED_PAD src0_sel:WORD_1
	v_cvt_f32_i32_sdwa v91, sext(v39) dst_sel:DWORD dst_unused:UNUSED_PAD src0_sel:WORD_1
	v_cvt_f32_i32_sdwa v90, sext(v37) dst_sel:DWORD dst_unused:UNUSED_PAD src0_sel:WORD_1
	v_cvt_f32_i32_sdwa v93, sext(v39) dst_sel:DWORD dst_unused:UNUSED_PAD src0_sel:WORD_0
	v_cvt_f32_i32_sdwa v92, sext(v37) dst_sel:DWORD dst_unused:UNUSED_PAD src0_sel:WORD_0
	v_pk_mul_f32 v[36:37], s[20:21], v[58:59]
	v_pk_mul_f32 v[38:39], s[20:21], v[60:61]
	v_add_f32_e32 v54, -1.0, v54
	v_cmp_lt_f32_e32 vcc, 0, v57
	v_mov_b32_e32 v58, v38
	v_mov_b32_e32 v59, v36
	v_cndmask_b32_e32 v57, v54, v57, vcc
	v_add_f32_e32 v53, -1.0, v53
	v_cmp_lt_f32_e32 vcc, 0, v56
	v_mov_b32_e32 v36, v39
	v_pk_add_f32 v[38:39], v[58:59], 0 op_sel_hi:[1,0]
	v_add_f32_e32 v59, v55, v52
	v_cndmask_b32_e32 v53, v53, v56, vcc
	v_add_f32_e32 v59, v59, v57
	v_add_f32_e32 v59, v59, v53
	v_mbcnt_lo_u32_b32 v54, -1, 0
	v_mbcnt_hi_u32_b32 v54, -1, v54
	v_add_f32_dpp v59, v59, v59 quad_perm:[1,0,3,2] row_mask:0xf bank_mask:0xf bound_ctrl:1
	v_and_b32_e32 v58, 64, v54
	v_xor_b32_e32 v56, 32, v54
	v_add_f32_dpp v59, v59, v59 quad_perm:[2,3,0,1] row_mask:0xf bank_mask:0xf bound_ctrl:1
	v_add_u32_e32 v58, 64, v58
	v_cmp_lt_i32_e32 vcc, v56, v58
	v_add_f32_dpp v59, v59, v59 row_half_mirror row_mask:0xf bank_mask:0xf bound_ctrl:1
	s_mov_b32 s74, s72
	v_cndmask_b32_e32 v54, v54, v56, vcc
	v_add_f32_dpp v59, v59, v59 row_mirror row_mask:0xf bank_mask:0xf bound_ctrl:1
	ds_swizzle_b32 v60, v59 offset:swizzle(SWAP,16)
	v_lshlrev_b32_e32 v54, 2, v54
	s_mov_b32 s75, s58
	v_pk_add_f32 v[36:37], v[38:39], v[36:37]
	v_pk_mul_f32 v[38:39], s[74:75], v[48:49]
	s_waitcnt lgkmcnt(0)
	v_add_f32_e32 v56, v59, v60
	ds_bpermute_b32 v60, v54, v56
	v_pk_mul_f32 v[48:49], s[74:75], v[64:65]
	v_mov_b32_e32 v59, v38
	v_mov_b32_e32 v58, v48
	v_mov_b32_e32 v38, v49
	s_waitcnt lgkmcnt(0)
	v_add_f32_e32 v48, v56, v60
	v_fmac_f32_e32 v52, 0xbb800000, v48
	v_fmac_f32_e32 v55, 0xbb800000, v48
	v_mul_f32_e32 v49, v52, v52
	v_fmac_f32_e32 v49, v55, v55
	v_fmac_f32_e32 v57, 0xbb800000, v48
	v_fmac_f32_e32 v49, v57, v57
	v_fmac_f32_e32 v53, 0xbb800000, v48
	v_fmac_f32_e32 v49, v53, v53
	v_pk_add_f32 v[36:37], v[36:37], v[58:59]
	s_mov_b32 s16, s66
	v_add_f32_dpp v48, v49, v49 quad_perm:[1,0,3,2] row_mask:0xf bank_mask:0xf bound_ctrl:1
	s_mov_b32 s17, s64
	v_pk_mul_f32 v[40:41], s[16:17], v[40:41]
	v_add_f32_dpp v48, v48, v48 quad_perm:[2,3,0,1] row_mask:0xf bank_mask:0xf bound_ctrl:1
	v_pk_add_f32 v[36:37], v[36:37], v[38:39]
	v_mov_b32_e32 v39, v40
	v_add_f32_dpp v48, v48, v48 row_half_mirror row_mask:0xf bank_mask:0xf bound_ctrl:1
	s_mov_b32 s18, s70
	s_mov_b32 s19, s46
	v_add_f32_dpp v56, v48, v48 row_mirror row_mask:0xf bank_mask:0xf bound_ctrl:1
	ds_swizzle_b32 v58, v56 offset:swizzle(SWAP,16)
	v_pk_mul_f32 v[48:49], s[16:17], v[68:69]
	v_pk_mul_f32 v[44:45], s[18:19], v[44:45]
	v_mov_b32_e32 v38, v48
	v_pk_add_f32 v[38:39], v[36:37], v[38:39]
	s_waitcnt lgkmcnt(0)
	v_add_f32_e32 v56, v56, v58
	ds_bpermute_b32 v58, v54, v56
	v_mov_b32_e32 v40, v49
	v_pk_mul_f32 v[48:49], s[18:19], v[88:89]
	v_pk_add_f32 v[38:39], v[38:39], v[40:41]
	v_mov_b32_e32 v40, v48
	v_mov_b32_e32 v41, v44
	s_waitcnt lgkmcnt(0)
	v_add_f32_e32 v56, v56, v58
	v_pk_add_f32 v[40:41], v[38:39], v[40:41]
	v_mov_b32_e32 v38, 0x3727c5ac
	v_fmamk_f32 v39, v56, 0x3b800000, v38
	v_rsq_f32_e32 v68, v39
	v_add_f32_e64 v39, s25, 0
	v_add_f32_e32 v39, s48, v39
	v_add_f32_e32 v39, s52, v39
	v_add_f32_e32 v39, s54, v39
	v_cvt_f32_i32_sdwa v63, sext(v51) dst_sel:DWORD dst_unused:UNUSED_PAD src0_sel:WORD_1
	v_cvt_f32_i32_sdwa v51, sext(v51) dst_sel:DWORD dst_unused:UNUSED_PAD src0_sel:WORD_0
	v_add_f32_e32 v39, s60, v39
	v_cvt_f32_i32_sdwa v67, sext(v43) dst_sel:DWORD dst_unused:UNUSED_PAD src0_sel:WORD_1
	v_add_f32_e32 v39, s56, v39
	v_cvt_f32_i32_sdwa v43, sext(v43) dst_sel:DWORD dst_unused:UNUSED_PAD src0_sel:WORD_0
	v_add_f32_e32 v39, s68, v39
	v_add_f32_e32 v39, s62, v39
	v_cvt_f32_i32_sdwa v87, sext(v47) dst_sel:DWORD dst_unused:UNUSED_PAD src0_sel:WORD_1
	v_cvt_f32_i32_sdwa v47, sext(v47) dst_sel:DWORD dst_unused:UNUSED_PAD src0_sel:WORD_0
	v_pk_mul_f32 v[58:59], s[20:21], v[62:63]
	v_pk_mul_f32 v[50:51], s[20:21], v[50:51]
	v_rcp_f32_e32 v48, v39
	v_pk_mul_f32 v[60:61], s[74:75], v[66:67]
	v_mov_b32_e32 v66, v58
	v_mov_b32_e32 v67, v50
	v_pk_mul_f32 v[42:43], s[74:75], v[42:43]
	v_mov_b32_e32 v44, v49
	v_mov_b32_e32 v50, v59
	v_pk_add_f32 v[58:59], v[66:67], 0 op_sel_hi:[1,0]
	v_pk_add_f32 v[40:41], v[40:41], v[44:45]
	v_pk_add_f32 v[50:51], v[58:59], v[50:51]
	v_mov_b32_e32 v58, v60
	v_mov_b32_e32 v59, v42
	v_pk_mul_f32 v[62:63], s[16:17], v[86:87]
	v_pk_mul_f32 v[46:47], s[16:17], v[46:47]
	v_pk_mul_f32 v[40:41], v[48:49], v[40:41] op_sel_hi:[0,1]
	v_pk_add_f32 v[50:51], v[50:51], v[58:59]
	v_mov_b32_e32 v42, v61
	v_mul_f32_e32 v39, 0x3fb8aa3b, v41
	v_mul_f32_e32 v49, 0x3fb8aa3b, v40
	v_pk_add_f32 v[42:43], v[50:51], v[42:43]
	v_mov_b32_e32 v50, v62
	v_mov_b32_e32 v51, v46
	v_pk_mul_f32 v[64:65], s[18:19], v[90:91]
	v_exp_f32_e32 v39, v39
	v_pk_mul_f32 v[44:45], s[18:19], v[92:93]
	v_exp_f32_e32 v49, v49
	v_pk_add_f32 v[42:43], v[42:43], v[50:51]
	v_mov_b32_e32 v46, v63
	v_pk_add_f32 v[42:43], v[42:43], v[46:47]
	v_mov_b32_e32 v46, v64
	v_mov_b32_e32 v47, v44
	global_load_dword v37, v2, s[28:29]
	global_load_dword v36, v2, s[30:31]
	v_pk_add_f32 v[42:43], v[42:43], v[46:47]
	v_mov_b32_e32 v44, v65
	v_pk_add_f32 v[42:43], v[42:43], v[44:45]
	v_add_f32_e32 v39, -1.0, v39
	v_cmp_lt_f32_e32 vcc, 0, v41
	v_pk_mul_f32 v[44:45], v[48:49], v[42:43] op_sel_hi:[0,1]
	v_mul_f32_e32 v42, 0x3fb8aa3b, v44
	v_cndmask_b32_e32 v69, v39, v41, vcc
	v_mul_f32_e32 v41, 0x3fb8aa3b, v45
	v_add_f32_e32 v39, -1.0, v49
	v_exp_f32_e32 v41, v41
	v_cmp_lt_f32_e32 vcc, 0, v40
	v_exp_f32_e32 v43, v42
	s_waitcnt vmcnt(16)
	v_cvt_f32_i32_sdwa v47, sext(v26) dst_sel:DWORD dst_unused:UNUSED_PAD src0_sel:WORD_1
	v_cndmask_b32_e32 v85, v39, v40, vcc
	global_load_dword v39, v2, s[28:29] offset:128
	global_load_dword v40, v2, s[30:31] offset:128
	v_add_f32_e32 v46, -1.0, v41
	global_load_dword v41, v2, s[28:29] offset:256
	global_load_dword v42, v2, s[30:31] offset:256
	v_cmp_lt_f32_e32 vcc, 0, v45
	v_add_f32_e32 v43, -1.0, v43
	s_mov_b32 s50, s22
	v_cndmask_b32_e32 v86, v46, v45, vcc
	v_cmp_lt_f32_e32 vcc, 0, v44
	v_cvt_f32_i32_sdwa v45, sext(v26) dst_sel:DWORD dst_unused:UNUSED_PAD src0_sel:WORD_0
	v_cvt_f32_i32_sdwa v46, sext(v24) dst_sel:DWORD dst_unused:UNUSED_PAD src0_sel:WORD_1
	v_cndmask_b32_e32 v87, v43, v44, vcc
	v_add_f32_e32 v43, v69, v85
	v_add_f32_e32 v43, v43, v86
	v_add_f32_e32 v43, v43, v87
	v_cvt_f32_i32_sdwa v44, sext(v24) dst_sel:DWORD dst_unused:UNUSED_PAD src0_sel:WORD_0
	v_cvt_f32_i32_sdwa v48, sext(v25) dst_sel:DWORD dst_unused:UNUSED_PAD src0_sel:WORD_1
	v_add_f32_dpp v43, v43, v43 quad_perm:[1,0,3,2] row_mask:0xf bank_mask:0xf bound_ctrl:1
	v_cvt_f32_i32_sdwa v26, sext(v25) dst_sel:DWORD dst_unused:UNUSED_PAD src0_sel:WORD_0
	v_pk_mul_f32 v[24:25], s[50:51], v[44:45]
	v_add_f32_dpp v43, v43, v43 quad_perm:[2,3,0,1] row_mask:0xf bank_mask:0xf bound_ctrl:1
	v_pk_mul_f32 v[44:45], s[50:51], v[46:47]
	s_waitcnt vmcnt(18)
	v_cvt_f32_i32_sdwa v47, sext(v22) dst_sel:DWORD dst_unused:UNUSED_PAD src0_sel:WORD_0
	v_add_f32_dpp v43, v43, v43 row_half_mirror row_mask:0xf bank_mask:0xf bound_ctrl:1
	v_cvt_f32_i32_sdwa v51, sext(v22) dst_sel:DWORD dst_unused:UNUSED_PAD src0_sel:WORD_1
	v_cvt_f32_i32_sdwa v58, sext(v21) dst_sel:DWORD dst_unused:UNUSED_PAD src0_sel:WORD_1
	v_add_f32_dpp v43, v43, v43 row_mirror row_mask:0xf bank_mask:0xf bound_ctrl:1
	ds_swizzle_b32 v56, v43 offset:swizzle(SWAP,16)
	v_cvt_f32_i32_sdwa v22, sext(v21) dst_sel:DWORD dst_unused:UNUSED_PAD src0_sel:WORD_0
	s_waitcnt vmcnt(16)
	v_cvt_f32_i32_sdwa v21, sext(v34) dst_sel:DWORD dst_unused:UNUSED_PAD src0_sel:WORD_0
	v_cvt_f32_i32_sdwa v61, sext(v34) dst_sel:DWORD dst_unused:UNUSED_PAD src0_sel:WORD_1
	v_cvt_f32_i32_sdwa v62, sext(v33) dst_sel:DWORD dst_unused:UNUSED_PAD src0_sel:WORD_1
	s_waitcnt lgkmcnt(0)
	v_add_f32_e32 v43, v43, v56
	v_cvt_f32_i32_sdwa v34, sext(v33) dst_sel:DWORD dst_unused:UNUSED_PAD src0_sel:WORD_0
	s_waitcnt vmcnt(14)
	v_cvt_f32_i32_sdwa v33, sext(v30) dst_sel:DWORD dst_unused:UNUSED_PAD src0_sel:WORD_0
	v_cvt_f32_i32_sdwa v65, sext(v30) dst_sel:DWORD dst_unused:UNUSED_PAD src0_sel:WORD_1
	v_cvt_f32_i32_sdwa v66, sext(v29) dst_sel:DWORD dst_unused:UNUSED_PAD src0_sel:WORD_1
	v_cvt_f32_i32_sdwa v30, sext(v29) dst_sel:DWORD dst_unused:UNUSED_PAD src0_sel:WORD_0
	v_mov_b32_e32 v29, v24
	v_mov_b32_e32 v24, v45
	ds_bpermute_b32 v45, v54, v43
	global_load_dword v88, v2, s[28:29] offset:384
	global_load_dword v89, v2, s[30:31] offset:384
	v_cvt_f32_i32_sdwa v46, sext(v20) dst_sel:DWORD dst_unused:UNUSED_PAD src0_sel:WORD_0
	v_cvt_f32_i32_sdwa v50, sext(v20) dst_sel:DWORD dst_unused:UNUSED_PAD src0_sel:WORD_1
	v_cvt_f32_i32_sdwa v20, sext(v32) dst_sel:DWORD dst_unused:UNUSED_PAD src0_sel:WORD_0
	s_waitcnt lgkmcnt(0)
	v_add_f32_e32 v43, v43, v45
	v_fmac_f32_e32 v85, 0xbb800000, v43
	v_fmac_f32_e32 v69, 0xbb800000, v43
	v_fmac_f32_e32 v86, 0xbb800000, v43
	v_fmac_f32_e32 v87, 0xbb800000, v43
	v_mul_f32_e32 v43, v85, v85
	v_fmac_f32_e32 v43, v69, v69
	v_fmac_f32_e32 v43, v86, v86
	v_fmac_f32_e32 v43, v87, v87
	v_cvt_f32_i32_sdwa v60, sext(v32) dst_sel:DWORD dst_unused:UNUSED_PAD src0_sel:WORD_1
	v_cvt_f32_i32_sdwa v32, sext(v28) dst_sel:DWORD dst_unused:UNUSED_PAD src0_sel:WORD_0
	v_add_f32_dpp v43, v43, v43 quad_perm:[1,0,3,2] row_mask:0xf bank_mask:0xf bound_ctrl:1
	v_cvt_f32_i32_sdwa v64, sext(v28) dst_sel:DWORD dst_unused:UNUSED_PAD src0_sel:WORD_1
	v_mov_b32_e32 v28, v44
	v_mul_f32_e32 v44, v68, v55
	v_add_f32_dpp v43, v43, v43 quad_perm:[2,3,0,1] row_mask:0xf bank_mask:0xf bound_ctrl:1
	v_mul_f32_e32 v45, v68, v52
	s_mov_b32 s58, s73
	v_add_f32_dpp v43, v43, v43 row_half_mirror row_mask:0xf bank_mask:0xf bound_ctrl:1
	v_pk_add_f32 v[28:29], v[28:29], 0 op_sel_hi:[1,0]
	s_waitcnt vmcnt(6)
	v_fma_f32 v44, v44, v37, v36
	v_add_f32_e32 v55, v44, v84
	v_add_f32_dpp v43, v43, v43 row_mirror row_mask:0xf bank_mask:0xf bound_ctrl:1
	v_cndmask_b32_e64 v55, v55, v44, s[4:5]
	ds_swizzle_b32 v44, v43 offset:swizzle(SWAP,16)
	v_pk_add_f32 v[24:25], v[28:29], v[24:25]
	v_cvt_f32_i32_sdwa v49, sext(v27) dst_sel:DWORD dst_unused:UNUSED_PAD src0_sel:WORD_1
	v_cvt_f32_i32_sdwa v59, sext(v23) dst_sel:DWORD dst_unused:UNUSED_PAD src0_sel:WORD_1
	s_mov_b32 s64, s67
	v_pk_mul_f32 v[20:21], s[64:65], v[20:21]
	s_mov_b32 s46, s71
	v_pk_mul_f32 v[32:33], s[46:47], v[32:33]
	v_cvt_f32_i32_sdwa v67, sext(v31) dst_sel:DWORD dst_unused:UNUSED_PAD src0_sel:WORD_1
	v_cvt_f32_i32_sdwa v31, sext(v31) dst_sel:DWORD dst_unused:UNUSED_PAD src0_sel:WORD_0
	v_cvt_f32_i32_sdwa v27, sext(v27) dst_sel:DWORD dst_unused:UNUSED_PAD src0_sel:WORD_0
	v_cvt_f32_i32_sdwa v23, sext(v23) dst_sel:DWORD dst_unused:UNUSED_PAD src0_sel:WORD_0
	s_waitcnt vmcnt(4)
	v_fma_f32 v45, v45, v39, v40
	v_add_f32_e32 v52, v45, v83
	v_cndmask_b32_e64 v56, v52, v45, s[4:5]
	s_waitcnt lgkmcnt(0)
	v_add_f32_e32 v52, v43, v44
	v_mul_f32_e32 v43, v68, v57
	s_waitcnt vmcnt(2)
	v_fma_f32 v43, v43, v41, v42
	v_add_f32_e32 v44, v43, v78
	v_cndmask_b32_e64 v57, v44, v43, s[4:5]
	v_pk_mul_f32 v[44:45], s[58:59], v[46:47]
	v_mul_f32_e32 v68, v68, v53
	v_mov_b32_e32 v29, v44
	v_add_f32_e64 v44, s26, 0
	v_add_f32_e32 v44, s49, v44
	ds_bpermute_b32 v53, v54, v52
	v_add_f32_e32 v44, s53, v44
	v_add_f32_e32 v44, s55, v44
	v_add_f32_e32 v44, s61, v44
	v_pk_mul_f32 v[46:47], s[58:59], v[50:51]
	v_add_f32_e32 v44, s57, v44
	v_mov_b32_e32 v28, v46
	v_add_f32_e32 v44, s69, v44
	v_pk_add_f32 v[24:25], v[24:25], v[28:29]
	s_waitcnt lgkmcnt(0)
	v_add_f32_e32 v28, v52, v53
	v_pk_mul_f32 v[50:51], s[64:65], v[60:61]
	v_add_f32_e32 v46, s63, v44
	v_mov_b32_e32 v44, v47
	v_fmamk_f32 v28, v28, 0x3b800000, v38
	v_pk_add_f32 v[24:25], v[24:25], v[44:45]
	v_mov_b32_e32 v44, v50
	v_mov_b32_e32 v45, v20
	v_rsq_f32_e32 v78, v28
	v_pk_mul_f32 v[28:29], s[50:51], v[48:49]
	v_pk_mul_f32 v[48:49], s[58:59], v[58:59]
	v_pk_mul_f32 v[58:59], s[46:47], v[64:65]
	v_rcp_f32_e32 v46, v46
	v_pk_add_f32 v[24:25], v[24:25], v[44:45]
	v_mov_b32_e32 v20, v51
	v_pk_add_f32 v[20:21], v[24:25], v[20:21]
	v_mov_b32_e32 v24, v58
	v_mov_b32_e32 v25, v32
	v_pk_add_f32 v[20:21], v[20:21], v[24:25]
	v_mov_b32_e32 v32, v59
	v_pk_add_f32 v[20:21], v[20:21], v[32:33]
	v_cvt_f32_i32_sdwa v63, sext(v35) dst_sel:DWORD dst_unused:UNUSED_PAD src0_sel:WORD_1
	v_pk_mul_f32 v[20:21], v[46:47], v[20:21] op_sel_hi:[0,1]
	v_mul_f32_e32 v24, 0x3fb8aa3b, v21
	v_exp_f32_e32 v32, v24
	v_pk_mul_f32 v[24:25], s[46:47], v[30:31]
	v_mul_f32_e32 v30, 0x3fb8aa3b, v20
	v_exp_f32_e32 v30, v30
	v_cvt_f32_i32_sdwa v35, sext(v35) dst_sel:DWORD dst_unused:UNUSED_PAD src0_sel:WORD_0
	v_pk_mul_f32 v[26:27], s[50:51], v[26:27]
	v_add_f32_e32 v31, -1.0, v32
	v_cmp_lt_f32_e32 vcc, 0, v21
	v_pk_mul_f32 v[22:23], s[58:59], v[22:23]
	v_pk_mul_f32 v[52:53], s[64:65], v[62:63]
	v_cndmask_b32_e32 v50, v31, v21, vcc
	v_add_f32_e32 v21, -1.0, v30
	v_mov_b32_e32 v30, v28
	v_mov_b32_e32 v31, v26
	v_pk_add_f32 v[30:31], v[30:31], 0 op_sel_hi:[1,0]
	v_mov_b32_e32 v26, v29
	v_pk_add_f32 v[26:27], v[30:31], v[26:27]
	v_mov_b32_e32 v28, v48
	v_mov_b32_e32 v29, v22
	v_pk_mul_f32 v[34:35], s[64:65], v[34:35]
	v_pk_add_f32 v[26:27], v[26:27], v[28:29]
	v_mov_b32_e32 v22, v49
	v_pk_add_f32 v[22:23], v[26:27], v[22:23]
	v_mov_b32_e32 v26, v52
	v_mov_b32_e32 v27, v34
	v_pk_mul_f32 v[60:61], s[46:47], v[66:67]
	v_pk_add_f32 v[22:23], v[22:23], v[26:27]
	v_mov_b32_e32 v34, v53
	v_pk_add_f32 v[22:23], v[22:23], v[34:35]
	v_mov_b32_e32 v26, v60
	v_mov_b32_e32 v27, v24
	v_pk_add_f32 v[22:23], v[22:23], v[26:27]
	v_mov_b32_e32 v24, v61
	v_pk_add_f32 v[22:23], v[22:23], v[24:25]
	v_cmp_lt_f32_e32 vcc, 0, v20
	v_pk_mul_f32 v[22:23], v[46:47], v[22:23] op_sel_hi:[0,1]
	v_mul_f32_e32 v24, 0x3fb8aa3b, v23
	v_exp_f32_e32 v24, v24
	v_cndmask_b32_e32 v48, v21, v20, vcc
	v_mul_f32_e32 v20, 0x3fb8aa3b, v22
	v_exp_f32_e32 v20, v20
	v_add_f32_e32 v21, -1.0, v24
	v_cmp_lt_f32_e32 vcc, 0, v23
	v_cvt_f32_i32_sdwa v25, sext(v19) dst_sel:DWORD dst_unused:UNUSED_PAD src0_sel:WORD_1
	v_add_f32_e32 v20, -1.0, v20
	v_cndmask_b32_e32 v49, v21, v23, vcc
	v_cmp_lt_f32_e32 vcc, 0, v22
	v_cvt_f32_i32_sdwa v24, sext(v17) dst_sel:DWORD dst_unused:UNUSED_PAD src0_sel:WORD_1
	v_add_f32_e64 v26, s27, 0
	v_cndmask_b32_e32 v51, v20, v22, vcc
	v_add_f32_e32 v20, v50, v48
	v_add_f32_e32 v20, v20, v49
	v_add_f32_e32 v20, v20, v51
	s_waitcnt vmcnt(0)
	v_fma_f32 v22, v68, v88, v89
	v_add_f32_e32 v23, v22, v74
	v_add_f32_dpp v20, v20, v20 quad_perm:[1,0,3,2] row_mask:0xf bank_mask:0xf bound_ctrl:1
	v_cndmask_b32_e64 v61, v23, v22, s[4:5]
	v_mul_f32_e32 v22, v78, v69
	v_add_f32_dpp v20, v20, v20 quad_perm:[2,3,0,1] row_mask:0xf bank_mask:0xf bound_ctrl:1
	v_fma_f32 v22, v22, v37, v36
	v_add_f32_e32 v23, v22, v77
	v_add_f32_dpp v20, v20, v20 row_half_mirror row_mask:0xf bank_mask:0xf bound_ctrl:1
	v_cndmask_b32_e64 v58, v23, v22, s[4:5]
	v_mul_f32_e32 v22, v78, v85
	v_add_f32_dpp v20, v20, v20 row_mirror row_mask:0xf bank_mask:0xf bound_ctrl:1
	ds_swizzle_b32 v21, v20 offset:swizzle(SWAP,16)
	v_fma_f32 v22, v22, v39, v40
	v_add_f32_e32 v23, v22, v76
	v_cndmask_b32_e64 v59, v23, v22, s[4:5]
	v_mul_f32_e32 v22, v78, v86
	s_waitcnt lgkmcnt(0)
	v_add_f32_e32 v20, v20, v21
	ds_bpermute_b32 v21, v54, v20
	v_fma_f32 v22, v22, v41, v42
	v_add_f32_e32 v23, v22, v75
	v_cndmask_b32_e64 v60, v23, v22, s[4:5]
	v_cvt_f32_i32_sdwa v23, sext(v18) dst_sel:DWORD dst_unused:UNUSED_PAD src0_sel:WORD_1
	s_waitcnt lgkmcnt(0)
	v_add_f32_e32 v20, v20, v21
	v_fmac_f32_e32 v48, 0xbb800000, v20
	v_fmac_f32_e32 v50, 0xbb800000, v20
	v_mul_f32_e32 v21, v48, v48
	v_fmac_f32_e32 v21, v50, v50
	v_fmac_f32_e32 v49, 0xbb800000, v20
	v_fmac_f32_e32 v21, v49, v49
	v_fmac_f32_e32 v51, 0xbb800000, v20
	v_fmac_f32_e32 v21, v51, v51
	v_cvt_f32_i32_sdwa v22, sext(v16) dst_sel:DWORD dst_unused:UNUSED_PAD src0_sel:WORD_1
	s_mov_b32 s44, s23
	v_add_f32_dpp v20, v21, v21 quad_perm:[1,0,3,2] row_mask:0xf bank_mask:0xf bound_ctrl:1
	v_cvt_f32_i32_sdwa v27, sext(v10) dst_sel:DWORD dst_unused:UNUSED_PAD src0_sel:WORD_1
	v_cvt_f32_i32_sdwa v29, sext(v11) dst_sel:DWORD dst_unused:UNUSED_PAD src0_sel:WORD_1
	v_add_f32_dpp v20, v20, v20 quad_perm:[2,3,0,1] row_mask:0xf bank_mask:0xf bound_ctrl:1
	v_cvt_f32_i32_sdwa v28, sext(v9) dst_sel:DWORD dst_unused:UNUSED_PAD src0_sel:WORD_1
	v_cvt_f32_i32_sdwa v31, sext(v14) dst_sel:DWORD dst_unused:UNUSED_PAD src0_sel:WORD_1
	v_add_f32_dpp v20, v20, v20 row_half_mirror row_mask:0xf bank_mask:0xf bound_ctrl:1
	v_cvt_f32_i32_sdwa v33, sext(v15) dst_sel:DWORD dst_unused:UNUSED_PAD src0_sel:WORD_1
	v_cvt_f32_i32_sdwa v32, sext(v13) dst_sel:DWORD dst_unused:UNUSED_PAD src0_sel:WORD_1
	v_add_f32_dpp v20, v20, v20 row_mirror row_mask:0xf bank_mask:0xf bound_ctrl:1
	ds_swizzle_b32 v21, v20 offset:swizzle(SWAP,16)
	v_cvt_f32_i32_sdwa v35, sext(v6) dst_sel:DWORD dst_unused:UNUSED_PAD src0_sel:WORD_1
	v_cvt_f32_i32_sdwa v19, sext(v19) dst_sel:DWORD dst_unused:UNUSED_PAD src0_sel:WORD_0
	v_cvt_f32_i32_sdwa v11, sext(v11) dst_sel:DWORD dst_unused:UNUSED_PAD src0_sel:WORD_0
	v_cvt_f32_i32_sdwa v15, sext(v15) dst_sel:DWORD dst_unused:UNUSED_PAD src0_sel:WORD_0
	s_waitcnt lgkmcnt(0)
	v_add_f32_e32 v20, v20, v21
	ds_bpermute_b32 v21, v54, v20
	v_cvt_f32_i32_sdwa v45, sext(v7) dst_sel:DWORD dst_unused:UNUSED_PAD src0_sel:WORD_1
	v_cvt_f32_i32_sdwa v44, sext(v5) dst_sel:DWORD dst_unused:UNUSED_PAD src0_sel:WORD_1
	v_cvt_f32_i32_sdwa v7, sext(v7) dst_sel:DWORD dst_unused:UNUSED_PAD src0_sel:WORD_0
	v_mul_f32_e32 v52, v78, v87
	s_waitcnt lgkmcnt(0)
	v_add_f32_e32 v20, v20, v21
	v_fmamk_f32 v20, v20, 0x3b800000, v38
	v_rsq_f32_e32 v53, v20
	v_cvt_f32_i32_sdwa v21, sext(v18) dst_sel:DWORD dst_unused:UNUSED_PAD src0_sel:WORD_0
	v_cvt_f32_i32_sdwa v20, sext(v16) dst_sel:DWORD dst_unused:UNUSED_PAD src0_sel:WORD_0
	v_cvt_f32_i32_sdwa v18, sext(v17) dst_sel:DWORD dst_unused:UNUSED_PAD src0_sel:WORD_0
	v_pk_mul_f32 v[44:45], s[38:39], v[44:45]
	v_readlane_b32 s2, v102, 2
	v_pk_mul_f32 v[16:17], s[44:45], v[20:21]
	v_pk_mul_f32 v[20:21], s[44:45], v[22:23]
	v_pk_mul_f32 v[22:23], s[44:45], v[24:25]
	v_add_f32_e32 v24, s97, v26
	v_add_f32_e32 v30, s98, v24
	v_cvt_f32_i32_sdwa v25, sext(v10) dst_sel:DWORD dst_unused:UNUSED_PAD src0_sel:WORD_0
	v_cvt_f32_i32_sdwa v24, sext(v8) dst_sel:DWORD dst_unused:UNUSED_PAD src0_sel:WORD_0
	v_cvt_f32_i32_sdwa v26, sext(v8) dst_sel:DWORD dst_unused:UNUSED_PAD src0_sel:WORD_1
	v_cvt_f32_i32_sdwa v10, sext(v9) dst_sel:DWORD dst_unused:UNUSED_PAD src0_sel:WORD_0
	v_mov_b32_e32 v47, v16
	v_pk_mul_f32 v[8:9], s[42:43], v[24:25]
	v_pk_mul_f32 v[24:25], s[42:43], v[26:27]
	v_pk_mul_f32 v[26:27], s[42:43], v[28:29]
	v_add_f32_e32 v28, s95, v30
	v_add_f32_e32 v34, s96, v28
	v_cvt_f32_i32_sdwa v29, sext(v14) dst_sel:DWORD dst_unused:UNUSED_PAD src0_sel:WORD_0
	v_cvt_f32_i32_sdwa v28, sext(v12) dst_sel:DWORD dst_unused:UNUSED_PAD src0_sel:WORD_0
	v_cvt_f32_i32_sdwa v30, sext(v12) dst_sel:DWORD dst_unused:UNUSED_PAD src0_sel:WORD_1
	v_add_f32_e32 v46, s94, v34
	v_cvt_f32_i32_sdwa v14, sext(v13) dst_sel:DWORD dst_unused:UNUSED_PAD src0_sel:WORD_0
	v_pk_mul_f32 v[12:13], s[40:41], v[28:29]
	v_pk_mul_f32 v[28:29], s[40:41], v[30:31]
	v_pk_mul_f32 v[30:31], s[40:41], v[32:33]
	v_cvt_f32_i32_sdwa v32, sext(v4) dst_sel:DWORD dst_unused:UNUSED_PAD src0_sel:WORD_0
	v_cvt_f32_i32_sdwa v34, sext(v4) dst_sel:DWORD dst_unused:UNUSED_PAD src0_sel:WORD_1
	v_add_f32_e32 v4, s93, v46
	v_mov_b32_e32 v46, v20
	v_cvt_f32_i32_sdwa v33, sext(v6) dst_sel:DWORD dst_unused:UNUSED_PAD src0_sel:WORD_0
	v_pk_add_f32 v[46:47], v[46:47], 0 op_sel_hi:[1,0]
	v_mov_b32_e32 v16, v21
	v_pk_add_f32 v[16:17], v[46:47], v[16:17]
	v_mov_b32_e32 v20, v24
	v_mov_b32_e32 v21, v8
	v_pk_add_f32 v[16:17], v[16:17], v[20:21]
	v_mov_b32_e32 v8, v25
	v_add_f32_e32 v4, s76, v4
	v_pk_add_f32 v[8:9], v[16:17], v[8:9]
	v_mov_b32_e32 v16, v28
	v_mov_b32_e32 v17, v12
	v_pk_mul_f32 v[32:33], s[38:39], v[32:33]
	v_pk_mul_f32 v[34:35], s[38:39], v[34:35]
	v_rcp_f32_e32 v4, v4
	v_pk_add_f32 v[8:9], v[8:9], v[16:17]
	v_mov_b32_e32 v12, v29
	v_pk_add_f32 v[8:9], v[8:9], v[12:13]
	v_mov_b32_e32 v12, v34
	v_mov_b32_e32 v13, v32
	v_pk_add_f32 v[8:9], v[8:9], v[12:13]
	v_mov_b32_e32 v32, v35
	v_pk_add_f32 v[8:9], v[8:9], v[32:33]
	v_pk_mul_f32 v[18:19], s[44:45], v[18:19]
	v_pk_mul_f32 v[8:9], v[4:5], v[8:9] op_sel_hi:[0,1]
	v_mul_f32_e32 v12, 0x3fb8aa3b, v8
	v_exp_f32_e32 v12, v12
	v_mov_b32_e32 v13, v18
	v_pk_mul_f32 v[10:11], s[42:43], v[10:11]
	v_cvt_f32_i32_sdwa v6, sext(v5) dst_sel:DWORD dst_unused:UNUSED_PAD src0_sel:WORD_0
	v_add_f32_e32 v20, -1.0, v12
	v_mov_b32_e32 v12, v22
	v_pk_add_f32 v[12:13], v[12:13], 0 op_sel_hi:[1,0]
	v_mov_b32_e32 v18, v23
	v_pk_add_f32 v[12:13], v[12:13], v[18:19]
	v_mov_b32_e32 v16, v26
	v_mov_b32_e32 v17, v10
	v_pk_mul_f32 v[14:15], s[40:41], v[14:15]
	v_mul_f32_e32 v5, 0x3fb8aa3b, v9
	v_pk_add_f32 v[12:13], v[12:13], v[16:17]
	v_mov_b32_e32 v10, v27
	v_exp_f32_e32 v5, v5
	v_pk_add_f32 v[10:11], v[12:13], v[10:11]
	v_mov_b32_e32 v12, v30
	v_mov_b32_e32 v13, v14
	v_pk_mul_f32 v[6:7], s[38:39], v[6:7]
	v_pk_add_f32 v[10:11], v[10:11], v[12:13]
	v_mov_b32_e32 v14, v31
	v_pk_add_f32 v[10:11], v[10:11], v[14:15]
	v_mov_b32_e32 v12, v44
	v_mov_b32_e32 v13, v6
	v_pk_add_f32 v[10:11], v[10:11], v[12:13]
	v_mov_b32_e32 v6, v45
	v_add_f32_e32 v5, -1.0, v5
	v_cmp_lt_f32_e32 vcc, 0, v9
	v_pk_add_f32 v[6:7], v[10:11], v[6:7]
	v_fma_f32 v10, v52, v88, v89
	v_cndmask_b32_e32 v9, v5, v9, vcc
	v_pk_mul_f32 v[4:5], v[4:5], v[6:7] op_sel_hi:[0,1]
	v_mul_f32_e32 v6, 0x3fb8aa3b, v5
	v_cmp_lt_f32_e32 vcc, 0, v8
	v_exp_f32_e32 v6, v6
	v_add_f32_e32 v3, v10, v3
	v_cndmask_b32_e32 v7, v20, v8, vcc
	v_mul_f32_e32 v8, 0x3fb8aa3b, v4
	v_exp_f32_e32 v8, v8
	v_add_f32_e32 v6, -1.0, v6
	v_cmp_lt_f32_e32 vcc, 0, v5
	v_cndmask_b32_e64 v78, v3, v10, s[4:5]
	v_mul_f32_e32 v3, v53, v50
	v_cndmask_b32_e32 v5, v6, v5, vcc
	v_add_f32_e32 v6, -1.0, v8
	v_cmp_lt_f32_e32 vcc, 0, v4
	v_fma_f32 v3, v3, v37, v36
	v_add_f32_e32 v10, v3, v73
	v_cndmask_b32_e32 v4, v6, v4, vcc
	v_add_f32_e32 v6, v9, v7
	v_add_f32_e32 v6, v6, v5
	v_add_f32_e32 v6, v6, v4
	v_cndmask_b32_e64 v63, v10, v3, s[4:5]
	v_mul_f32_e32 v3, v53, v48
	v_add_f32_dpp v6, v6, v6 quad_perm:[1,0,3,2] row_mask:0xf bank_mask:0xf bound_ctrl:1
	v_fma_f32 v3, v3, v39, v40
	v_add_f32_e32 v10, v3, v72
	v_add_f32_dpp v6, v6, v6 quad_perm:[2,3,0,1] row_mask:0xf bank_mask:0xf bound_ctrl:1
	v_cndmask_b32_e64 v75, v10, v3, s[4:5]
	v_mul_f32_e32 v3, v53, v49
	v_add_f32_dpp v6, v6, v6 row_half_mirror row_mask:0xf bank_mask:0xf bound_ctrl:1
	v_fma_f32 v3, v3, v41, v42
	v_add_f32_e32 v10, v3, v71
	v_add_f32_dpp v6, v6, v6 row_mirror row_mask:0xf bank_mask:0xf bound_ctrl:1
	ds_swizzle_b32 v8, v6 offset:swizzle(SWAP,16)
	v_cndmask_b32_e64 v76, v10, v3, s[4:5]
	v_mul_f32_e32 v3, v53, v51
	v_fma_f32 v3, v3, v88, v89
	s_mul_i32 s3, s2, 0x1040
	s_waitcnt lgkmcnt(0)
	v_add_f32_e32 v6, v6, v8
	ds_bpermute_b32 v8, v54, v6
	v_mov_b32_e32 v43, 0
	s_lshl_b32 s6, s2, 4
	s_waitcnt lgkmcnt(0)
	v_add_f32_e32 v6, v6, v8
	v_fmac_f32_e32 v7, 0xbb800000, v6
	v_fmac_f32_e32 v9, 0xbb800000, v6
	v_mul_f32_e32 v8, v7, v7
	v_fmac_f32_e32 v8, v9, v9
	v_fmac_f32_e32 v5, 0xbb800000, v6
	v_fmac_f32_e32 v8, v5, v5
	v_fmac_f32_e32 v4, 0xbb800000, v6
	v_fmac_f32_e32 v8, v4, v4
	s_nop 1
	v_add_f32_dpp v6, v8, v8 quad_perm:[1,0,3,2] row_mask:0xf bank_mask:0xf bound_ctrl:1
	s_nop 1
	v_add_f32_dpp v6, v6, v6 quad_perm:[2,3,0,1] row_mask:0xf bank_mask:0xf bound_ctrl:1
	s_nop 1
	v_add_f32_dpp v6, v6, v6 row_half_mirror row_mask:0xf bank_mask:0xf bound_ctrl:1
	s_nop 1
	v_add_f32_dpp v6, v6, v6 row_mirror row_mask:0xf bank_mask:0xf bound_ctrl:1
	ds_swizzle_b32 v8, v6 offset:swizzle(SWAP,16)
	s_waitcnt lgkmcnt(0)
	v_add_f32_e32 v6, v6, v8
	ds_bpermute_b32 v8, v54, v6
	s_waitcnt lgkmcnt(0)
	v_add_f32_e32 v6, v6, v8
	v_fmac_f32_e32 v38, 0x3b800000, v6
	v_rsq_f32_e32 v6, v38
	v_add_f32_e32 v8, v3, v70
	v_cndmask_b32_e64 v77, v8, v3, s[4:5]
	global_load_dword v71, v2, s[12:13]
	global_load_dword v67, v2, s[12:13] offset:1024
	global_load_dword v73, v2, s[12:13] offset:128
	global_load_dword v70, v2, s[12:13] offset:1152
	global_load_dword v72, v2, s[12:13] offset:256
	global_load_dword v68, v2, s[12:13] offset:1280
	global_load_dword v69, v2, s[12:13] offset:1408
	global_load_dword v74, v2, s[12:13] offset:384
	v_mul_f32_e32 v3, v6, v9
	v_fmac_f32_e32 v36, v3, v37
	v_add_f32_e32 v3, v36, v82
	v_cndmask_b32_e64 v62, v3, v36, s[4:5]
	v_mul_f32_e32 v3, v6, v7
	v_fmac_f32_e32 v40, v3, v39
	v_add_f32_e32 v3, v40, v81
	v_cndmask_b32_e64 v64, v3, v40, s[4:5]
	v_mul_f32_e32 v3, v6, v5
	v_fmac_f32_e32 v42, v3, v41
	v_add_f32_e32 v3, v42, v80
	v_cndmask_b32_e64 v65, v3, v42, s[4:5]
	v_mul_f32_e32 v3, v6, v4
	v_fmac_f32_e32 v89, v3, v88
	v_add_f32_e32 v3, v89, v79
	v_add_u32_e32 v2, s3, v2
	v_cndmask_b32_e64 v66, v3, v89, s[4:5]
	v_add_u32_e32 v3, 0x400, v2
	ds_write2_b32 v2, v55, v56 offset1:32
	ds_write2_b32 v2, v57, v61 offset0:64 offset1:96
	ds_write2_b32 v3, v58, v59 offset0:4 offset1:36
	ds_write2_b32 v3, v60, v78 offset0:68 offset1:100
	v_add_u32_e32 v3, 0x800, v2
	v_add_u32_e32 v2, 0xc00, v2
	ds_write2_b32 v3, v63, v75 offset0:8 offset1:40
	ds_write2_b32 v3, v76, v77 offset0:72 offset1:104
	ds_write2_b32 v2, v62, v64 offset0:12 offset1:44
	ds_write2_b32 v2, v65, v66 offset0:76 offset1:108
	v_lshlrev_b32_e32 v2, 4, v0
	v_and_b32_e32 v42, 0x3f0, v2
	v_lshrrev_b32_e32 v2, 6, v0
	v_or_b32_e32 v6, s92, v2
	s_movk_i32 s3, 0x410
	v_ashrrev_i32_e32 v7, 31, v6
	v_mad_u32_u24 v10, v2, s3, v42
	v_lshlrev_b64 v[8:9], 10, v[6:7]
	s_waitcnt lgkmcnt(0)
	s_barrier
	s_lshl_b64 s[4:5], s[6:7], 10
	s_add_u32 s100, s8, s4
	s_addc_u32 s101, s9, s5
	s_add_u32 s4, s10, s4
	s_addc_u32 s5, s11, s5
	v_lshlrev_b32_e32 v103, 4, v1
	global_load_dwordx4 v[18:21], v103, s[100:101]
	global_load_dwordx4 v[22:25], v103, s[4:5]
	global_load_dwordx4 v[26:29], v103, s[100:101] offset:1024
	global_load_dwordx4 v[30:33], v103, s[4:5] offset:1024
	global_load_dwordx4 v[82:85], v103, s[4:5] offset:2048
	global_load_dwordx4 v[50:53], v103, s[100:101] offset:2048
	ds_read_b128 v[2:5], v10
	v_lshl_add_u64 v[8:9], s[36:37], 0, v[8:9]
	v_lshl_add_u64 v[8:9], v[8:9], 0, v[42:43]
	s_waitcnt lgkmcnt(0)
	global_store_dwordx4 v[8:9], v[2:5], off sc0 sc1
	s_nop 1
	v_or_b32_e32 v2, 0x200, v0
	v_lshrrev_b32_e32 v2, 6, v2
	v_or_b32_e32 v8, s92, v2
	v_ashrrev_i32_e32 v9, 31, v8
	v_lshlrev_b64 v[8:9], 10, v[8:9]
	v_or_b32_e32 v6, 16, v6
	v_mad_u32_u24 v3, v2, s3, v42
	v_lshl_add_u64 v[8:9], s[36:37], 0, v[8:9]
	v_ashrrev_i32_e32 v7, 31, v6
	ds_read_b128 v[2:5], v3
	v_lshl_add_u64 v[8:9], v[8:9], 0, v[42:43]
	s_waitcnt lgkmcnt(0)
	global_store_dwordx4 v[8:9], v[2:5], off sc0 sc1
	s_nop 1
	v_lshlrev_b64 v[6:7], 10, v[6:7]
	ds_read_b128 v[2:5], v10 offset:16640
	v_lshl_add_u64 v[6:7], s[36:37], 0, v[6:7]
	v_lshl_add_u64 v[6:7], v[6:7], 0, v[42:43]
	s_waitcnt lgkmcnt(0)
	global_store_dwordx4 v[6:7], v[2:5], off sc0 sc1
	s_nop 1
	v_or_b32_e32 v2, 0x600, v0
	v_lshrrev_b32_e32 v2, 6, v2
	v_add_u32_e32 v6, s92, v2
	v_ashrrev_i32_e32 v7, 31, v6
	v_lshlrev_b64 v[6:7], 10, v[6:7]
	s_lshl_b64 s[4:5], s[6:7], 10
	v_mad_u32_u24 v3, v2, s3, v42
	v_lshl_add_u64 v[6:7], s[36:37], 0, v[6:7]
	s_add_u32 s6, s8, s4
	ds_read_b128 v[2:5], v3
	v_lshl_add_u64 v[6:7], v[6:7], 0, v[42:43]
	s_waitcnt lgkmcnt(0)
	global_store_dwordx4 v[6:7], v[2:5], off sc0 sc1
	s_nop 1
	s_addc_u32 s7, s9, s5
	v_lshlrev_b32_e32 v42, 4, v1
	s_add_u32 s4, s10, s4
	s_addc_u32 s5, s11, s5
	v_lshrrev_b32_e32 v2, 2, v0
	v_and_b32_e32 v80, 8, v2
	v_and_b32_e32 v79, 31, v0
	v_lshlrev_b32_e32 v2, 2, v80
	v_mad_u32_u24 v81, v79, s3, v2
	ds_read_b128 v[2:5], v81
	ds_read_b128 v[34:37], v81 offset:16
	s_movk_i32 s3, 0x2000
	ds_read_b128 v[86:89], v81 offset:192
	ds_read_b128 v[90:93], v81 offset:208
	s_waitcnt lgkmcnt(3)
	v_cvt_f16_f32_e32 v6, v2
	v_cvt_f16_f32_e32 v7, v3
	v_cvt_pk_f16_f32 v39, v4, v5
	v_cvt_pk_f16_f32 v38, v2, v3
	v_cvt_f32_f16_e32 v6, v6
	v_cvt_f32_f16_e32 v9, v7
	v_cvt_f32_f16_sdwa v7, v39 dst_sel:DWORD dst_unused:UNUSED_PAD src0_sel:WORD_1
	s_waitcnt lgkmcnt(2)
	v_cvt_pk_f16_f32 v40, v34, v35
	v_sub_f32_e32 v8, v2, v6
	v_cvt_f32_f16_e32 v6, v39
	v_sub_f32_e32 v2, v3, v9
	v_cvt_pk_f16_f32 v41, v36, v37
	v_cvt_pk_f16_f32 v44, v8, v2
	v_pk_add_f32 v[2:3], v[4:5], v[6:7] neg_lo:[0,1] neg_hi:[0,1]
	v_cvt_f32_f16_e32 v4, v40
	v_cvt_f32_f16_sdwa v5, v40 dst_sel:DWORD dst_unused:UNUSED_PAD src0_sel:WORD_1
	v_cvt_f32_f16_e32 v48, v41
	v_cvt_f32_f16_sdwa v49, v41 dst_sel:DWORD dst_unused:UNUSED_PAD src0_sel:WORD_1
	v_cvt_pk_f16_f32 v45, v2, v3
	v_pk_add_f32 v[34:35], v[34:35], v[4:5] neg_lo:[0,1] neg_hi:[0,1]
	s_waitcnt vmcnt(9)
	v_mfma_f32_32x32x16_f16 v[2:17], v[38:41], v[18:21], 0
	v_cvt_pk_f16_f32 v46, v34, v35
	v_add_f32_e64 v34, v36, -v48
	v_add_f32_e64 v35, v37, -v49
	v_cvt_pk_f16_f32 v47, v34, v35
	ds_read_b128 v[34:37], v81 offset:64
	s_nop 0
	v_mfma_f32_32x32x16_f16 v[2:17], v[44:47], v[18:21], v[2:17]
	ds_read_b128 v[18:21], v81 offset:80
	s_waitcnt lgkmcnt(1)
	v_cvt_f16_f32_e32 v44, v34
	v_cvt_f16_f32_e32 v45, v35
	v_cvt_f32_f16_e32 v44, v44
	s_waitcnt vmcnt(8)
	v_mfma_f32_32x32x16_f16 v[2:17], v[38:41], v[22:25], v[2:17]
	v_cvt_pk_f16_f32 v23, v36, v37
	v_cvt_f32_f16_e32 v39, v45
	v_cvt_f32_f16_e32 v24, v23
	v_cvt_f32_f16_sdwa v25, v23 dst_sel:DWORD dst_unused:UNUSED_PAD src0_sel:WORD_1
	v_sub_f32_e32 v38, v34, v44
	v_cvt_pk_f16_f32 v22, v34, v35
	v_sub_f32_e32 v34, v35, v39
	v_pk_add_f32 v[36:37], v[36:37], v[24:25] neg_lo:[0,1] neg_hi:[0,1]
	s_waitcnt lgkmcnt(0)
	v_cvt_pk_f16_f32 v24, v18, v19
	v_cvt_pk_f16_f32 v34, v38, v34
	v_cvt_f32_f16_e32 v38, v24
	v_cvt_f32_f16_sdwa v39, v24 dst_sel:DWORD dst_unused:UNUSED_PAD src0_sel:WORD_1
	v_cvt_pk_f16_f32 v25, v20, v21
	v_cvt_f32_f16_e32 v40, v25
	v_cvt_f32_f16_sdwa v41, v25 dst_sel:DWORD dst_unused:UNUSED_PAD src0_sel:WORD_1
	v_pk_add_f32 v[18:19], v[18:19], v[38:39] neg_lo:[0,1] neg_hi:[0,1]
	v_cvt_pk_f16_f32 v35, v36, v37
	s_waitcnt vmcnt(7)
	v_mfma_f32_32x32x16_f16 v[2:17], v[22:25], v[26:29], v[2:17]
	v_cvt_pk_f16_f32 v36, v18, v19
	v_add_f32_e64 v18, v20, -v40
	v_add_f32_e64 v19, v21, -v41
	global_load_dwordx4 v[38:41], v42, s[6:7] offset:3072
	v_cvt_pk_f16_f32 v37, v18, v19
	ds_read_b128 v[18:21], v81 offset:128
	v_lshl_add_u64 v[44:45], s[6:7], 0, v[42:43]
	v_add_co_u32_e32 v48, vcc, s3, v44
	v_mfma_f32_32x32x16_f16 v[2:17], v[34:37], v[26:29], v[2:17]
	ds_read_b128 v[26:29], v81 offset:144
	s_waitcnt lgkmcnt(1)
	v_cvt_f16_f32_e32 v34, v18
	v_cvt_f16_f32_e32 v35, v19
	v_addc_co_u32_e32 v49, vcc, 0, v45, vcc
	v_cvt_f32_f16_e32 v34, v34
	v_cvt_f32_f16_e32 v35, v35
	s_waitcnt vmcnt(7)
	v_mfma_f32_32x32x16_f16 v[2:17], v[22:25], v[30:33], v[2:17]
	v_cvt_pk_f16_f32 v31, v20, v21
	v_cvt_f32_f16_e32 v32, v31
	v_cvt_f32_f16_sdwa v33, v31 dst_sel:DWORD dst_unused:UNUSED_PAD src0_sel:WORD_1
	v_sub_f32_e32 v34, v18, v34
	global_load_dwordx4 v[22:25], v42, s[4:5] offset:3072
	v_cvt_pk_f16_f32 v30, v18, v19
	v_sub_f32_e32 v18, v19, v35
	v_cvt_pk_f16_f32 v34, v34, v18
	v_pk_add_f32 v[18:19], v[20:21], v[32:33] neg_lo:[0,1] neg_hi:[0,1]
	s_waitcnt lgkmcnt(0)
	v_cvt_pk_f16_f32 v32, v26, v27
	v_cvt_f32_f16_e32 v20, v32
	v_cvt_f32_f16_sdwa v21, v32 dst_sel:DWORD dst_unused:UNUSED_PAD src0_sel:WORD_1
	v_cvt_pk_f16_f32 v33, v28, v29
	v_cvt_f32_f16_e32 v46, v33
	v_cvt_f32_f16_sdwa v47, v33 dst_sel:DWORD dst_unused:UNUSED_PAD src0_sel:WORD_1
	v_cvt_pk_f16_f32 v35, v18, v19
	v_pk_add_f32 v[18:19], v[26:27], v[20:21] neg_lo:[0,1] neg_hi:[0,1]
	s_waitcnt vmcnt(6)
	v_mfma_f32_32x32x16_f16 v[2:17], v[30:33], v[50:53], v[2:17]
	v_cvt_pk_f16_f32 v36, v18, v19
	v_add_f32_e64 v18, v28, -v46
	v_add_f32_e64 v19, v29, -v47
	v_cvt_f16_f32_e32 v26, v86
	v_cvt_pk_f16_f32 v37, v18, v19
	global_load_dwordx4 v[18:21], v[48:49], off offset:-4096
	v_cvt_f16_f32_e32 v27, v87
	v_lshl_add_u64 v[46:47], s[4:5], 0, v[42:43]
	v_mfma_f32_32x32x16_f16 v[2:17], v[34:37], v[50:53], v[2:17]
	v_add_co_u32_e32 v50, vcc, s3, v46
	v_cvt_f32_f16_e32 v34, v26
	s_nop 0
	v_addc_co_u32_e32 v51, vcc, 0, v47, vcc
	v_cvt_pk_f16_f32 v35, v88, v89
	s_movk_i32 s3, 0x1000
	v_mfma_f32_32x32x16_f16 v[2:17], v[30:33], v[82:85], v[2:17]
	v_cvt_f32_f16_e32 v32, v27
	global_load_dwordx4 v[26:29], v[50:51], off offset:-4096
	v_cvt_f32_f16_e32 v30, v35
	v_cvt_f32_f16_sdwa v31, v35 dst_sel:DWORD dst_unused:UNUSED_PAD src0_sel:WORD_1
	v_add_co_u32_e32 v52, vcc, s3, v44
	v_sub_f32_e32 v33, v86, v34
	v_sub_f32_e32 v32, v87, v32
	v_pk_add_f32 v[30:31], v[88:89], v[30:31] neg_lo:[0,1] neg_hi:[0,1]
	v_addc_co_u32_e32 v53, vcc, 0, v45, vcc
	v_cvt_pk_f16_f32 v82, v33, v32
	v_cvt_pk_f16_f32 v83, v30, v31
	global_load_dwordx4 v[30:33], v[52:53], off offset:1024
	v_cvt_pk_f16_f32 v34, v86, v87
	v_cvt_pk_f16_f32 v36, v90, v91
	v_cvt_pk_f16_f32 v37, v92, v93
	v_cvt_f32_f16_e32 v84, v36
	v_cvt_f32_f16_sdwa v85, v36 dst_sel:DWORD dst_unused:UNUSED_PAD src0_sel:WORD_1
	v_cvt_f32_f16_e32 v86, v37
	v_cvt_f32_f16_sdwa v87, v37 dst_sel:DWORD dst_unused:UNUSED_PAD src0_sel:WORD_1
	s_waitcnt vmcnt(4)
	v_mfma_f32_32x32x16_f16 v[2:17], v[34:37], v[38:41], v[2:17]
	v_add_f32_e64 v84, v90, -v84
	v_add_f32_e64 v85, v91, -v85
	v_add_f32_e64 v86, v92, -v86
	v_add_f32_e64 v87, v93, -v87
	v_cvt_pk_f16_f32 v84, v84, v85
	v_cvt_pk_f16_f32 v85, v86, v87
	v_add_co_u32_e32 v98, vcc, s3, v46
	s_movk_i32 s3, 0x3000
	v_mfma_f32_32x32x16_f16 v[2:17], v[82:85], v[38:41], v[2:17]
	ds_read_b128 v[82:85], v81 offset:256
	ds_read_b128 v[38:41], v81 offset:272
	v_addc_co_u32_e32 v99, vcc, 0, v47, vcc
	global_load_dwordx4 v[86:89], v[98:99], off offset:1024
	s_waitcnt lgkmcnt(1)
	v_cvt_f16_f32_e32 v90, v83
	v_cvt_f16_f32_e32 v42, v82
	s_movk_i32 s6, 0x50
	s_waitcnt vmcnt(4)
	v_mfma_f32_32x32x16_f16 v[2:17], v[34:37], v[22:25], v[2:17]
	v_cvt_f32_f16_e32 v90, v90
	v_cvt_f32_f16_e32 v42, v42
	v_cvt_pk_f16_f32 v35, v84, v85
	v_cvt_pk_f16_f32 v34, v82, v83
	v_sub_f32_e32 v25, v83, v90
	global_load_dwordx4 v[90:93], v[52:53], off offset:2048
	s_waitcnt lgkmcnt(0)
	v_cvt_pk_f16_f32 v36, v38, v39
	v_cvt_pk_f16_f32 v37, v40, v41
	v_sub_f32_e32 v24, v82, v42
	v_cvt_pk_f16_f32 v82, v24, v25
	v_cvt_f32_f16_e32 v24, v36
	v_cvt_f32_f16_sdwa v25, v36 dst_sel:DWORD dst_unused:UNUSED_PAD src0_sel:WORD_1
	v_cvt_f32_f16_e32 v22, v35
	v_cvt_f32_f16_sdwa v23, v35 dst_sel:DWORD dst_unused:UNUSED_PAD src0_sel:WORD_1
	v_cvt_f32_f16_e32 v94, v37
	v_cvt_f32_f16_sdwa v95, v37 dst_sel:DWORD dst_unused:UNUSED_PAD src0_sel:WORD_1
	s_waitcnt vmcnt(4)
	v_mfma_f32_32x32x16_f16 v[2:17], v[34:37], v[18:21], v[2:17]
	v_add_f32_e64 v38, v38, -v24
	v_add_f32_e64 v39, v39, -v25
	v_add_f32_e64 v22, v84, -v22
	v_add_f32_e64 v23, v85, -v23
	v_cvt_pk_f16_f32 v84, v38, v39
	v_pk_add_f32 v[38:39], v[40:41], v[94:95] neg_lo:[0,1] neg_hi:[0,1]
	v_cvt_pk_f16_f32 v83, v22, v23
	v_cvt_pk_f16_f32 v85, v38, v39
	global_load_dwordx4 v[38:41], v[98:99], off offset:2048
	global_load_dwordx4 v[22:25], v[48:49], off
	v_mfma_f32_32x32x16_f16 v[2:17], v[82:85], v[18:21], v[2:17]
	ds_read_b128 v[18:21], v81 offset:320
	ds_read_b128 v[82:85], v81 offset:336
	global_load_dwordx4 v[94:97], v[50:51], off
	s_ashr_i32 s4, s92, 6
	s_ashr_i32 s5, s4, 31
	s_waitcnt lgkmcnt(1)
	v_cvt_f16_f32_e32 v42, v18
	v_cvt_f16_f32_e32 v100, v19
	s_waitcnt vmcnt(6)
	v_mfma_f32_32x32x16_f16 v[2:17], v[34:37], v[26:29], v[2:17]
	v_cvt_pk_f16_f32 v27, v20, v21
	v_cvt_f32_f16_e32 v26, v42
	v_cvt_f32_f16_e32 v34, v100
	v_cvt_f32_f16_e32 v28, v27
	v_cvt_f32_f16_sdwa v29, v27 dst_sel:DWORD dst_unused:UNUSED_PAD src0_sel:WORD_1
	v_sub_f32_e32 v35, v18, v26
	v_cvt_pk_f16_f32 v26, v18, v19
	v_sub_f32_e32 v18, v19, v34
	v_cvt_pk_f16_f32 v18, v35, v18
	global_load_dwordx4 v[34:37], v[52:53], off offset:3072
	v_pk_add_f32 v[20:21], v[20:21], v[28:29] neg_lo:[0,1] neg_hi:[0,1]
	s_waitcnt lgkmcnt(0)
	v_cvt_pk_f16_f32 v28, v82, v83
	v_cvt_pk_f16_f32 v29, v84, v85
	v_cvt_f32_f16_e32 v100, v28
	v_cvt_f32_f16_sdwa v101, v28 dst_sel:DWORD dst_unused:UNUSED_PAD src0_sel:WORD_1
	v_cvt_f32_f16_e32 v52, v29
	v_cvt_f32_f16_sdwa v53, v29 dst_sel:DWORD dst_unused:UNUSED_PAD src0_sel:WORD_1
	s_waitcnt vmcnt(6)
	v_mfma_f32_32x32x16_f16 v[2:17], v[26:29], v[30:33], v[2:17]
	v_cvt_pk_f16_f32 v19, v20, v21
	v_add_f32_e64 v20, v82, -v100
	v_add_f32_e64 v21, v83, -v101
	v_add_f32_e64 v52, v84, -v52
	v_add_f32_e64 v53, v85, -v53
	v_cvt_pk_f16_f32 v20, v20, v21
	v_cvt_pk_f16_f32 v21, v52, v53
	ds_read_b128 v[82:85], v81 offset:400
	s_and_b32 s7, s92, 32
	v_mfma_f32_32x32x16_f16 v[2:17], v[18:21], v[30:33], v[2:17]
	global_load_dwordx4 v[30:33], v[98:99], off offset:3072
	ds_read_b128 v[18:21], v81 offset:384
	s_lshl_b64 s[4:5], s[4:5], 8
	s_waitcnt lgkmcnt(0)
	v_cvt_f16_f32_e32 v42, v18
	s_waitcnt vmcnt(6)
	v_mfma_f32_32x32x16_f16 v[2:17], v[26:29], v[86:89], v[2:17]
	v_cvt_f16_f32_e32 v52, v19
	v_cvt_f32_f16_e32 v26, v42
	v_cvt_pk_f16_f32 v27, v20, v21
	v_cvt_pk_f16_f32 v28, v82, v83
	v_cvt_pk_f16_f32 v29, v84, v85
	v_sub_f32_e32 v98, v18, v26
	v_cvt_pk_f16_f32 v26, v18, v19
	v_cvt_f32_f16_e32 v42, v52
	v_cvt_f32_f16_e32 v52, v27
	v_cvt_f32_f16_sdwa v53, v27 dst_sel:DWORD dst_unused:UNUSED_PAD src0_sel:WORD_1
	v_cvt_f32_f16_e32 v86, v28
	v_cvt_f32_f16_sdwa v87, v28 dst_sel:DWORD dst_unused:UNUSED_PAD src0_sel:WORD_1
	v_cvt_f32_f16_e32 v88, v29
	v_cvt_f32_f16_sdwa v89, v29 dst_sel:DWORD dst_unused:UNUSED_PAD src0_sel:WORD_1
	s_waitcnt vmcnt(5)
	v_mfma_f32_32x32x16_f16 v[2:17], v[26:29], v[90:93], v[2:17]
	v_sub_f32_e32 v18, v19, v42
	v_add_f32_e64 v20, v20, -v52
	v_add_f32_e64 v21, v21, -v53
	v_add_f32_e64 v52, v82, -v86
	v_add_f32_e64 v53, v83, -v87
	v_pk_add_f32 v[82:83], v[84:85], v[88:89] neg_lo:[0,1] neg_hi:[0,1]
	v_cvt_pk_f16_f32 v18, v98, v18
	v_cvt_pk_f16_f32 v19, v20, v21
	v_cvt_pk_f16_f32 v20, v52, v53
	v_cvt_pk_f16_f32 v21, v82, v83
	s_nop 1
	v_mfma_f32_32x32x16_f16 v[2:17], v[18:21], v[90:93], v[2:17]
	ds_read_b128 v[18:21], v81 offset:448
	ds_read_b128 v[82:85], v81 offset:464
	s_waitcnt lgkmcnt(1)
	v_cvt_f16_f32_e32 v42, v18
	v_cvt_f16_f32_e32 v52, v19
	s_waitcnt vmcnt(4)
	v_mfma_f32_32x32x16_f16 v[2:17], v[26:29], v[38:41], v[2:17]
	v_cvt_f32_f16_e32 v26, v42
	v_cvt_f32_f16_e32 v38, v52
	v_cvt_pk_f16_f32 v27, v20, v21
	v_cvt_f32_f16_e32 v28, v27
	v_sub_f32_e32 v39, v18, v26
	v_cvt_pk_f16_f32 v26, v18, v19
	v_sub_f32_e32 v18, v19, v38
	v_cvt_f32_f16_sdwa v29, v27 dst_sel:DWORD dst_unused:UNUSED_PAD src0_sel:WORD_1
	v_cvt_pk_f16_f32 v18, v39, v18
	global_load_dwordx4 v[38:41], v[48:49], off offset:1024
	v_pk_add_f32 v[20:21], v[20:21], v[28:29] neg_lo:[0,1] neg_hi:[0,1]
	s_waitcnt lgkmcnt(0)
	v_cvt_pk_f16_f32 v28, v82, v83
	v_cvt_pk_f16_f32 v29, v84, v85
	v_cvt_f32_f16_e32 v52, v28
	v_cvt_f32_f16_sdwa v53, v28 dst_sel:DWORD dst_unused:UNUSED_PAD src0_sel:WORD_1
	v_cvt_f32_f16_e32 v86, v29
	v_cvt_f32_f16_sdwa v87, v29 dst_sel:DWORD dst_unused:UNUSED_PAD src0_sel:WORD_1
	s_waitcnt vmcnt(2)
	v_mfma_f32_32x32x16_f16 v[2:17], v[26:29], v[34:37], v[2:17]
	v_cvt_pk_f16_f32 v19, v20, v21
	v_add_f32_e64 v20, v82, -v52
	v_add_f32_e64 v21, v83, -v53
	v_add_f32_e64 v52, v84, -v86
	v_add_f32_e64 v53, v85, -v87
	v_cvt_pk_f16_f32 v20, v20, v21
	v_cvt_pk_f16_f32 v21, v52, v53
	ds_read_b128 v[82:85], v81 offset:528
	s_nop 0
	v_mfma_f32_32x32x16_f16 v[2:17], v[18:21], v[34:37], v[2:17]
	ds_read_b128 v[18:21], v81 offset:512
	global_load_dwordx4 v[34:37], v[50:51], off offset:1024
	s_waitcnt lgkmcnt(0)
	v_cvt_f16_f32_e32 v42, v18
	v_cvt_f16_f32_e32 v52, v19
	s_waitcnt vmcnt(2)
	v_mfma_f32_32x32x16_f16 v[2:17], v[26:29], v[30:33], v[2:17]
	v_cvt_pk_f16_f32 v27, v20, v21
	v_cvt_f32_f16_e32 v26, v42
	v_cvt_f32_f16_e32 v30, v52
	v_cvt_f32_f16_e32 v28, v27
	v_cvt_f32_f16_sdwa v29, v27 dst_sel:DWORD dst_unused:UNUSED_PAD src0_sel:WORD_1
	v_sub_f32_e32 v31, v18, v26
	v_cvt_pk_f16_f32 v26, v18, v19
	v_sub_f32_e32 v18, v19, v30
	v_cvt_pk_f16_f32 v18, v31, v18
	global_load_dwordx4 v[30:33], v[48:49], off offset:2048
	v_pk_add_f32 v[20:21], v[20:21], v[28:29] neg_lo:[0,1] neg_hi:[0,1]
	v_cvt_pk_f16_f32 v28, v82, v83
	v_cvt_pk_f16_f32 v29, v84, v85
	v_cvt_f32_f16_e32 v52, v28
	v_cvt_f32_f16_sdwa v53, v28 dst_sel:DWORD dst_unused:UNUSED_PAD src0_sel:WORD_1
	v_cvt_pk_f16_f32 v19, v20, v21
	v_cvt_f32_f16_e32 v20, v29
	v_cvt_f32_f16_sdwa v21, v29 dst_sel:DWORD dst_unused:UNUSED_PAD src0_sel:WORD_1
	v_mfma_f32_32x32x16_f16 v[2:17], v[26:29], v[22:25], v[2:17]
	v_add_f32_e64 v52, v82, -v52
	v_add_f32_e64 v53, v83, -v53
	v_add_f32_e64 v82, v84, -v20
	v_add_f32_e64 v83, v85, -v21
	v_cvt_pk_f16_f32 v20, v52, v53
	v_cvt_pk_f16_f32 v21, v82, v83
	s_nop 1
	v_mfma_f32_32x32x16_f16 v[2:17], v[18:21], v[22:25], v[2:17]
	ds_read_b128 v[18:21], v81 offset:576
	ds_read_b128 v[22:25], v81 offset:592
	global_load_dwordx4 v[82:85], v[50:51], off offset:2048
	global_load_dwordx4 v[86:89], v[48:49], off offset:3072
	s_waitcnt lgkmcnt(1)
	v_cvt_f16_f32_e32 v42, v18
	v_cvt_f16_f32_e32 v52, v19
	v_mfma_f32_32x32x16_f16 v[2:17], v[26:29], v[94:97], v[2:17]
	v_cvt_pk_f16_f32 v27, v20, v21
	v_cvt_f32_f16_e32 v26, v42
	v_cvt_f32_f16_e32 v28, v27
	v_cvt_f32_f16_sdwa v29, v27 dst_sel:DWORD dst_unused:UNUSED_PAD src0_sel:WORD_1
	v_cvt_f32_f16_e32 v42, v52
	v_sub_f32_e32 v52, v18, v26
	v_cvt_pk_f16_f32 v26, v18, v19
	v_pk_add_f32 v[20:21], v[20:21], v[28:29] neg_lo:[0,1] neg_hi:[0,1]
	s_waitcnt lgkmcnt(0)
	v_cvt_pk_f16_f32 v28, v22, v23
	v_cvt_pk_f16_f32 v29, v24, v25
	v_sub_f32_e32 v18, v19, v42
	v_cvt_pk_f16_f32 v18, v52, v18
	v_cvt_pk_f16_f32 v19, v20, v21
	v_cvt_f32_f16_e32 v20, v28
	v_cvt_f32_f16_sdwa v21, v28 dst_sel:DWORD dst_unused:UNUSED_PAD src0_sel:WORD_1
	v_cvt_f32_f16_e32 v52, v29
	v_cvt_f32_f16_sdwa v53, v29 dst_sel:DWORD dst_unused:UNUSED_PAD src0_sel:WORD_1
	s_waitcnt vmcnt(4)
	v_mfma_f32_32x32x16_f16 v[2:17], v[26:29], v[38:41], v[2:17]
	v_add_f32_e64 v20, v22, -v20
	v_add_f32_e64 v21, v23, -v21
	v_add_f32_e64 v22, v24, -v52
	v_add_f32_e64 v23, v25, -v53
	v_cvt_pk_f16_f32 v20, v20, v21
	v_cvt_pk_f16_f32 v21, v22, v23
	ds_read_b128 v[22:25], v81 offset:640
	s_nop 0
	v_mfma_f32_32x32x16_f16 v[2:17], v[18:21], v[38:41], v[2:17]
	ds_read_b128 v[18:21], v81 offset:656
	s_waitcnt lgkmcnt(1)
	v_cvt_f16_f32_e32 v38, v22
	v_cvt_f16_f32_e32 v42, v23
	v_cvt_f32_f16_e32 v48, v38
	global_load_dwordx4 v[38:41], v[50:51], off offset:3072
	s_waitcnt vmcnt(4)
	v_mfma_f32_32x32x16_f16 v[2:17], v[26:29], v[34:37], v[2:17]
	v_cvt_f32_f16_e32 v28, v42
	v_sub_f32_e32 v29, v22, v48
	v_cvt_pk_f16_f32 v34, v22, v23
	v_cvt_pk_f16_f32 v35, v24, v25
	v_sub_f32_e32 v22, v23, v28
	v_add_co_u32_e32 v28, vcc, s3, v44
	v_cvt_pk_f16_f32 v22, v29, v22
	s_nop 0
	v_addc_co_u32_e32 v29, vcc, 0, v45, vcc
	global_load_dwordx4 v[48:51], v[28:29], off
	v_cvt_f32_f16_e32 v26, v35
	v_cvt_f32_f16_sdwa v27, v35 dst_sel:DWORD dst_unused:UNUSED_PAD src0_sel:WORD_1
	s_waitcnt lgkmcnt(0)
	v_cvt_pk_f16_f32 v36, v18, v19
	v_cvt_pk_f16_f32 v37, v20, v21
	v_cvt_f32_f16_e32 v44, v37
	v_pk_add_f32 v[24:25], v[24:25], v[26:27] neg_lo:[0,1] neg_hi:[0,1]
	v_cvt_f32_f16_e32 v26, v36
	v_cvt_f32_f16_sdwa v27, v36 dst_sel:DWORD dst_unused:UNUSED_PAD src0_sel:WORD_1
	v_cvt_f32_f16_sdwa v45, v37 dst_sel:DWORD dst_unused:UNUSED_PAD src0_sel:WORD_1
	s_waitcnt vmcnt(4)
	v_mfma_f32_32x32x16_f16 v[2:17], v[34:37], v[30:33], v[2:17]
	v_cvt_pk_f16_f32 v23, v24, v25
	v_add_f32_e64 v18, v18, -v26
	v_add_f32_e64 v19, v19, -v27
	v_add_f32_e64 v20, v20, -v44
	v_add_f32_e64 v21, v21, -v45
	v_cvt_pk_f16_f32 v24, v18, v19
	v_cvt_pk_f16_f32 v25, v20, v21
	v_add_co_u32_e32 v26, vcc, s3, v46
	s_nop 0
	v_mfma_f32_32x32x16_f16 v[2:17], v[22:25], v[30:33], v[2:17]
	v_addc_co_u32_e32 v27, vcc, 0, v47, vcc
	global_load_dwordx4 v[30:33], v[26:27], off
	ds_read_b128 v[18:21], v81 offset:704
	ds_read_b128 v[22:25], v81 offset:720
	s_mul_i32 s3, s2, 0xa00
	s_add_i32 s3, s3, 0x8200
	s_waitcnt vmcnt(4)
	v_mfma_f32_32x32x16_f16 v[2:17], v[34:37], v[82:85], v[2:17]
	s_waitcnt lgkmcnt(1)
	v_cvt_f16_f32_e32 v42, v18
	v_cvt_f16_f32_e32 v44, v19
	v_cvt_pk_f16_f32 v35, v20, v21
	v_cvt_f32_f16_e32 v36, v35
	v_cvt_f32_f16_e32 v34, v42
	v_cvt_f32_f16_e32 v42, v44
	v_cvt_f32_f16_sdwa v37, v35 dst_sel:DWORD dst_unused:UNUSED_PAD src0_sel:WORD_1
	s_lshl_b32 s2, s2, 5
	v_sub_f32_e32 v44, v18, v34
	v_cvt_pk_f16_f32 v34, v18, v19
	v_sub_f32_e32 v18, v19, v42
	v_pk_add_f32 v[46:47], v[20:21], v[36:37] neg_lo:[0,1] neg_hi:[0,1]
	v_cvt_pk_f16_f32 v44, v44, v18
	s_waitcnt lgkmcnt(0)
	v_cvt_pk_f16_f32 v36, v22, v23
	v_cvt_pk_f16_f32 v37, v24, v25
	global_load_dwordx4 v[18:21], v[28:29], off offset:1024
	v_cvt_f32_f16_e32 v52, v36
	v_cvt_f32_f16_sdwa v53, v36 dst_sel:DWORD dst_unused:UNUSED_PAD src0_sel:WORD_1
	v_cvt_f32_f16_e32 v82, v37
	v_cvt_f32_f16_sdwa v83, v37 dst_sel:DWORD dst_unused:UNUSED_PAD src0_sel:WORD_1
	s_waitcnt vmcnt(4)
	v_mfma_f32_32x32x16_f16 v[2:17], v[34:37], v[86:89], v[2:17]
	v_add_f32_e64 v22, v22, -v52
	v_add_f32_e64 v23, v23, -v53
	v_cvt_pk_f16_f32 v45, v46, v47
	v_add_f32_e64 v24, v24, -v82
	v_add_f32_e64 v25, v25, -v83
	v_cvt_pk_f16_f32 v46, v22, v23
	v_cvt_pk_f16_f32 v47, v24, v25
	global_load_dwordx4 v[22:25], v[26:27], off offset:1024
	ds_read_b128 v[82:85], v81 offset:784
	v_mfma_f32_32x32x16_f16 v[2:17], v[44:47], v[86:89], v[2:17]
	ds_read_b128 v[44:47], v81 offset:768
	s_add_u32 s4, s4, s2
	s_addc_u32 s5, s5, 0
	s_lshl_b32 s2, s7, 1
	s_add_u32 s2, s14, s2
	s_waitcnt lgkmcnt(0)
	v_cvt_f16_f32_e32 v42, v44
	v_cvt_f16_f32_e32 v52, v45
	s_waitcnt vmcnt(4)
	v_mfma_f32_32x32x16_f16 v[2:17], v[34:37], v[38:41], v[2:17]
	v_cvt_pk_f16_f32 v35, v46, v47
	v_cvt_f32_f16_e32 v34, v42
	v_cvt_f32_f16_e32 v38, v52
	v_cvt_f32_f16_e32 v36, v35
	v_cvt_f32_f16_sdwa v37, v35 dst_sel:DWORD dst_unused:UNUSED_PAD src0_sel:WORD_1
	v_sub_f32_e32 v39, v44, v34
	v_cvt_pk_f16_f32 v34, v44, v45
	v_sub_f32_e32 v38, v45, v38
	v_pk_add_f32 v[40:41], v[46:47], v[36:37] neg_lo:[0,1] neg_hi:[0,1]
	global_load_dwordx4 v[44:47], v[28:29], off offset:2048
	v_cvt_pk_f16_f32 v36, v82, v83
	v_cvt_pk_f16_f32 v37, v84, v85
	v_cvt_f32_f16_e32 v52, v36
	v_cvt_f32_f16_sdwa v53, v36 dst_sel:DWORD dst_unused:UNUSED_PAD src0_sel:WORD_1
	v_cvt_f32_f16_e32 v86, v37
	v_cvt_f32_f16_sdwa v87, v37 dst_sel:DWORD dst_unused:UNUSED_PAD src0_sel:WORD_1
	s_waitcnt vmcnt(4)
	v_mfma_f32_32x32x16_f16 v[2:17], v[34:37], v[48:51], v[2:17]
	v_cvt_pk_f16_f32 v38, v39, v38
	v_cvt_pk_f16_f32 v39, v40, v41
	v_add_f32_e64 v40, v82, -v52
	v_add_f32_e64 v41, v83, -v53
	v_add_f32_e64 v52, v84, -v86
	v_add_f32_e64 v53, v85, -v87
	v_cvt_pk_f16_f32 v40, v40, v41
	v_cvt_pk_f16_f32 v41, v52, v53
	v_cmp_eq_u32_e32 vcc, 0, v1
	s_nop 0
	v_mfma_f32_32x32x16_f16 v[2:17], v[38:41], v[48:51], v[2:17]
	global_load_dwordx4 v[38:41], v[26:27], off offset:2048
	ds_read_b128 v[48:51], v81 offset:832
	ds_read_b128 v[82:85], v81 offset:848
	s_waitcnt lgkmcnt(1)
	v_cvt_f16_f32_e32 v42, v48
	v_cvt_f16_f32_e32 v52, v49
	s_waitcnt vmcnt(4)
	v_mfma_f32_32x32x16_f16 v[2:17], v[34:37], v[30:33], v[2:17]
	v_cvt_pk_f16_f32 v31, v50, v51
	v_cvt_f32_f16_e32 v30, v42
	v_cvt_f32_f16_e32 v34, v52
	v_cvt_f32_f16_e32 v32, v31
	v_cvt_f32_f16_sdwa v33, v31 dst_sel:DWORD dst_unused:UNUSED_PAD src0_sel:WORD_1
	v_sub_f32_e32 v42, v48, v30
	v_cvt_pk_f16_f32 v30, v48, v49
	v_sub_f32_e32 v48, v49, v34
	global_load_dwordx4 v[34:37], v[28:29], off offset:3072
	v_pk_add_f32 v[50:51], v[50:51], v[32:33] neg_lo:[0,1] neg_hi:[0,1]
	s_waitcnt lgkmcnt(0)
	v_cvt_pk_f16_f32 v32, v82, v83
	v_cvt_f32_f16_e32 v28, v32
	v_cvt_f32_f16_sdwa v29, v32 dst_sel:DWORD dst_unused:UNUSED_PAD src0_sel:WORD_1
	v_cvt_pk_f16_f32 v33, v84, v85
	v_cvt_f32_f16_e32 v52, v33
	v_cvt_f32_f16_sdwa v53, v33 dst_sel:DWORD dst_unused:UNUSED_PAD src0_sel:WORD_1
	v_pk_add_f32 v[28:29], v[82:83], v[28:29] neg_lo:[0,1] neg_hi:[0,1]
	v_cvt_pk_f16_f32 v49, v50, v51
	v_cvt_pk_f16_f32 v50, v28, v29
	v_pk_add_f32 v[28:29], v[84:85], v[52:53] neg_lo:[0,1] neg_hi:[0,1]
	s_waitcnt vmcnt(4)
	v_mfma_f32_32x32x16_f16 v[2:17], v[30:33], v[18:21], v[2:17]
	v_cvt_pk_f16_f32 v51, v28, v29
	global_load_dwordx4 v[26:29], v[26:27], off offset:3072
	v_cvt_pk_f16_f32 v48, v42, v48
	ds_read_b128 v[82:85], v81 offset:896
	s_nop 0
	v_mfma_f32_32x32x16_f16 v[2:17], v[48:51], v[18:21], v[2:17]
	ds_read_b128 v[18:21], v81 offset:912
	s_waitcnt lgkmcnt(1)
	v_cvt_f16_f32_e32 v42, v82
	v_cvt_f16_f32_e32 v48, v83
	v_cvt_f32_f16_e32 v42, v42
	s_waitcnt vmcnt(4)
	v_mfma_f32_32x32x16_f16 v[2:17], v[30:33], v[22:25], v[2:17]
	v_cvt_pk_f16_f32 v23, v84, v85
	v_cvt_f32_f16_e32 v24, v23
	v_cvt_f32_f16_sdwa v25, v23 dst_sel:DWORD dst_unused:UNUSED_PAD src0_sel:WORD_1
	v_cvt_pk_f16_f32 v22, v82, v83
	v_cvt_f32_f16_e32 v31, v48
	v_sub_f32_e32 v30, v82, v42
	v_pk_add_f32 v[32:33], v[84:85], v[24:25] neg_lo:[0,1] neg_hi:[0,1]
	s_waitcnt lgkmcnt(0)
	v_cvt_pk_f16_f32 v24, v18, v19
	v_cvt_pk_f16_f32 v25, v20, v21
	v_cvt_f32_f16_e32 v48, v24
	v_cvt_f32_f16_sdwa v49, v24 dst_sel:DWORD dst_unused:UNUSED_PAD src0_sel:WORD_1
	v_cvt_f32_f16_e32 v50, v25
	v_cvt_f32_f16_sdwa v51, v25 dst_sel:DWORD dst_unused:UNUSED_PAD src0_sel:WORD_1
	s_waitcnt vmcnt(3)
	v_mfma_f32_32x32x16_f16 v[2:17], v[22:25], v[44:47], v[2:17]
	v_sub_f32_e32 v31, v83, v31
	v_add_f32_e64 v18, v18, -v48
	v_add_f32_e64 v19, v19, -v49
	v_cvt_pk_f16_f32 v30, v30, v31
	v_cvt_pk_f16_f32 v31, v32, v33
	v_cvt_pk_f16_f32 v32, v18, v19
	v_pk_add_f32 v[18:19], v[20:21], v[50:51] neg_lo:[0,1] neg_hi:[0,1]
	s_nop 0
	v_cvt_pk_f16_f32 v33, v18, v19
	ds_read_b128 v[18:21], v81 offset:960
	s_nop 0
	v_mfma_f32_32x32x16_f16 v[2:17], v[30:33], v[44:47], v[2:17]
	ds_read_b128 v[30:33], v81 offset:976
	s_waitcnt lgkmcnt(1)
	v_cvt_f16_f32_e32 v42, v18
	v_cvt_f16_f32_e32 v44, v19
	v_cvt_f32_f16_e32 v42, v42
	s_waitcnt vmcnt(2)
	v_mfma_f32_32x32x16_f16 v[2:17], v[22:25], v[38:41], v[2:17]
	v_cvt_pk_f16_f32 v23, v20, v21
	v_cvt_f32_f16_e32 v24, v23
	v_cvt_f32_f16_sdwa v25, v23 dst_sel:DWORD dst_unused:UNUSED_PAD src0_sel:WORD_1
	v_cvt_f32_f16_e32 v39, v44
	v_cvt_pk_f16_f32 v22, v18, v19
	v_sub_f32_e32 v38, v18, v42
	v_pk_add_f32 v[20:21], v[20:21], v[24:25] neg_lo:[0,1] neg_hi:[0,1]
	s_waitcnt lgkmcnt(0)
	v_cvt_pk_f16_f32 v24, v30, v31
	v_cvt_pk_f16_f32 v25, v32, v33
	v_sub_f32_e32 v18, v19, v39
	v_cvt_pk_f16_f32 v18, v38, v18
	v_cvt_f32_f16_e32 v38, v24
	v_cvt_f32_f16_sdwa v39, v24 dst_sel:DWORD dst_unused:UNUSED_PAD src0_sel:WORD_1
	v_cvt_f32_f16_e32 v40, v25
	v_cvt_f32_f16_sdwa v41, v25 dst_sel:DWORD dst_unused:UNUSED_PAD src0_sel:WORD_1
	s_waitcnt vmcnt(1)
	v_mfma_f32_32x32x16_f16 v[2:17], v[22:25], v[34:37], v[2:17]
	v_cvt_pk_f16_f32 v19, v20, v21
	v_add_f32_e64 v20, v30, -v38
	v_add_f32_e64 v21, v31, -v39
	v_add_f32_e64 v30, v32, -v40
	v_add_f32_e64 v31, v33, -v41
	v_cvt_pk_f16_f32 v20, v20, v21
	v_cvt_pk_f16_f32 v21, v30, v31
	s_nop 1
	v_mfma_f32_32x32x16_f16 v[2:17], v[18:21], v[34:37], v[2:17]
	v_mov_b32_e32 v18, s3
	v_mad_u32_u24 v18, v79, s6, v18
	v_or_b32_e32 v18, v18, v80
	s_waitcnt vmcnt(0)
	v_mfma_f32_32x32x16_f16 v[2:17], v[22:25], v[26:29], v[2:17]
	s_nop 11
	v_cvt_pk_f16_f32 v5, v4, v5
	v_cvt_pk_f16_f32 v4, v2, v3
	v_cvt_pk_f16_f32 v3, v8, v9
	v_cvt_pk_f16_f32 v2, v6, v7
	ds_write2_b64 v18, v[4:5], v[2:3] offset1:2
	v_cvt_pk_f16_f32 v3, v12, v13
	v_cvt_pk_f16_f32 v2, v10, v11
	v_cvt_pk_f16_f32 v5, v16, v17
	v_cvt_pk_f16_f32 v4, v14, v15
	ds_write2_b64 v18, v[2:3], v[4:5] offset0:4 offset1:6
	v_and_b32_e32 v2, 3, v0
	v_lshlrev_b32_e32 v42, 4, v2
	v_lshrrev_b32_e32 v3, 2, v1
	v_or_b32_e32 v2, s3, v42
	v_or_b32_e32 v6, s4, v3
	v_mov_b32_e32 v7, s5
	s_addc_u32 s3, s15, 0
	v_mad_u32_u24 v10, v3, s6, v2
	v_lshlrev_b64 v[8:9], 7, v[6:7]
	ds_read_b128 v[2:5], v10
	v_lshl_add_u64 v[8:9], s[2:3], 0, v[8:9]
	v_lshl_add_u64 v[8:9], v[8:9], 0, v[42:43]
	s_waitcnt lgkmcnt(0)
	global_store_dwordx4 v[8:9], v[2:5], off sc0 sc1
	s_nop 1
	v_mul_f32_e32 v4, v56, v73
	v_fmac_f32_e32 v4, v55, v71
	v_fmac_f32_e32 v4, v57, v72
	v_fmac_f32_e32 v4, v61, v74
	v_mul_f32_e32 v5, v56, v70
	v_fmac_f32_e32 v5, v55, v67
	v_add_f32_dpp v4, v4, v4 quad_perm:[1,0,3,2] row_mask:0xf bank_mask:0xf bound_ctrl:1
	v_fmac_f32_e32 v5, v57, v68
	v_fmac_f32_e32 v5, v61, v69
	v_add_f32_dpp v4, v4, v4 quad_perm:[2,3,0,1] row_mask:0xf bank_mask:0xf bound_ctrl:1
	v_or_b32_e32 v6, 16, v6
	v_lshlrev_b64 v[2:3], 7, v[6:7]
	v_add_f32_dpp v4, v4, v4 row_half_mirror row_mask:0xf bank_mask:0xf bound_ctrl:1
	v_lshl_add_u64 v[2:3], s[2:3], 0, v[2:3]
	v_lshl_add_u64 v[8:9], v[2:3], 0, v[42:43]
	v_add_f32_dpp v11, v4, v4 row_mirror row_mask:0xf bank_mask:0xf bound_ctrl:1
	v_add_f32_dpp v4, v5, v5 quad_perm:[1,0,3,2] row_mask:0xf bank_mask:0xf bound_ctrl:1
	ds_swizzle_b32 v12, v11 offset:swizzle(SWAP,16)
	s_waitcnt lgkmcnt(0)
	v_add_f32_e32 v2, v11, v12
	v_add_f32_dpp v4, v4, v4 quad_perm:[2,3,0,1] row_mask:0xf bank_mask:0xf bound_ctrl:1
	ds_bpermute_b32 v3, v54, v2
	s_nop 0
	v_add_f32_dpp v4, v4, v4 row_half_mirror row_mask:0xf bank_mask:0xf bound_ctrl:1
	s_nop 1
	v_add_f32_dpp v13, v4, v4 row_mirror row_mask:0xf bank_mask:0xf bound_ctrl:1
	ds_swizzle_b32 v14, v13 offset:swizzle(SWAP,16)
	ds_read_b128 v[4:7], v10 offset:1280
	s_waitcnt lgkmcnt(0)
	global_store_dwordx4 v[8:9], v[4:7], off sc0 sc1
	s_nop 1
	v_add_f32_e32 v10, v13, v14
	ds_bpermute_b32 v11, v54, v10
	s_waitcnt lgkmcnt(0)
	v_add_f32_e32 v1, v10, v11
	s_and_saveexec_b64 s[4:5], vcc
	s_load_dwordx4 s[8:11], s[0:1], 0x60
	s_cbranch_execz .LBB3_10
	s_waitcnt lgkmcnt(0)
	s_add_u32 s2, s10, s34
	s_addc_u32 s3, s11, s35
	s_add_u32 s6, s8, s34
	s_addc_u32 s7, s9, s35
	v_add_f32_e32 v2, v2, v3
	global_store_dword v43, v2, s[6:7]
	global_store_dword v43, v1, s[2:3]

	.amdhsa_kernel _Z9k_redprepILi1EEvPKfPKjS1_S1_S1_S1_S1_PfPKDv8_DF16_S7_S1_PDF16_S4_S4_S4_PKiS7_S1_S1_S1_S4_S4_
		.amdhsa_group_segment_fixed_size 53792
		.amdhsa_private_segment_fixed_size 0
		.amdhsa_kernarg_size 176
		.amdhsa_user_sgpr_count 2
		.amdhsa_user_sgpr_dispatch_ptr 0
		.amdhsa_user_sgpr_queue_ptr 0
		.amdhsa_user_sgpr_kernarg_segment_ptr 1
		.amdhsa_user_sgpr_dispatch_id 0
		.amdhsa_user_sgpr_kernarg_preload_length 0
		.amdhsa_user_sgpr_kernarg_preload_offset 0
		.amdhsa_user_sgpr_private_segment_size 0
		.amdhsa_uses_dynamic_stack 0
		.amdhsa_enable_private_segment 0
		.amdhsa_system_sgpr_workgroup_id_x 1
		.amdhsa_system_sgpr_workgroup_id_y 0
		.amdhsa_system_sgpr_workgroup_id_z 0
		.amdhsa_system_sgpr_workgroup_info 0
		.amdhsa_system_vgpr_workitem_id 0
		.amdhsa_next_free_vgpr 104
		.amdhsa_next_free_sgpr 102
		.amdhsa_accum_offset 104
		.amdhsa_reserve_vcc 1
		.amdhsa_float_round_mode_32 0
		.amdhsa_float_round_mode_16_64 0
		.amdhsa_float_denorm_mode_32 3
		.amdhsa_float_denorm_mode_16_64 3
		.amdhsa_dx10_clamp 1
		.amdhsa_ieee_mode 1
		.amdhsa_fp16_overflow 0
		.amdhsa_tg_split 0
		.amdhsa_exception_fp_ieee_invalid_op 0
		.amdhsa_exception_fp_denorm_src 0
		.amdhsa_exception_fp_ieee_div_zero 0
		.amdhsa_exception_fp_ieee_overflow 0
		.amdhsa_exception_fp_ieee_underflow 0
		.amdhsa_exception_fp_ieee_inexact 0
		.amdhsa_exception_int_div_zero 0
	.end_amdhsa_kernel

amdhsa.kernels:
  - .agpr_count:     0
    .args:
      - .actual_access:  read_only
        .address_space:  global
        .offset:         0
        .size:           8
        .value_kind:     global_buffer
      - .address_space:  global
        .offset:         8
        .size:           8
        .value_kind:     global_buffer
      - .actual_access:  read_only
        .address_space:  global
        .offset:         16
        .size:           8
        .value_kind:     global_buffer
      - .actual_access:  read_only
        .address_space:  global
        .offset:         24
        .size:           8
        .value_kind:     global_buffer
      - .actual_access:  read_only
        .address_space:  global
        .offset:         32
        .size:           8
        .value_kind:     global_buffer
      - .actual_access:  read_only
        .address_space:  global
        .offset:         40
        .size:           8
        .value_kind:     global_buffer
      - .actual_access:  read_only
        .address_space:  global
        .offset:         48
        .size:           8
        .value_kind:     global_buffer
      - .actual_access:  read_only
        .address_space:  global
        .offset:         56
        .size:           8
        .value_kind:     global_buffer
      - .actual_access:  write_only
        .address_space:  global
        .offset:         64
        .size:           8
        .value_kind:     global_buffer
      - .actual_access:  write_only
        .address_space:  global
        .offset:         72
        .size:           8
        .value_kind:     global_buffer
      - .actual_access:  write_only
        .address_space:  global
        .offset:         80
        .size:           8
        .value_kind:     global_buffer
      - .actual_access:  write_only
        .address_space:  global
        .offset:         88
        .size:           8
        .value_kind:     global_buffer
      - .actual_access:  read_only
        .address_space:  global
        .offset:         96
        .size:           8
        .value_kind:     global_buffer
      - .actual_access:  write_only
        .address_space:  global
        .offset:         104
        .size:           8
        .value_kind:     global_buffer
      - .actual_access:  read_only
        .address_space:  global
        .offset:         112
        .size:           8
        .value_kind:     global_buffer
      - .actual_access:  write_only
        .address_space:  global
        .offset:         120
        .size:           8
        .value_kind:     global_buffer
      - .actual_access:  write_only
        .address_space:  global
        .offset:         128
        .size:           8
        .value_kind:     global_buffer
      - .actual_access:  write_only
        .address_space:  global
        .offset:         136
        .size:           8
        .value_kind:     global_buffer
      - .actual_access:  write_only
        .address_space:  global
        .offset:         144
        .size:           8
        .value_kind:     global_buffer
    .group_segment_fixed_size: 4096
    .kernarg_segment_align: 8
    .kernarg_segment_size: 152
    .language:       OpenCL C
    .language_version:
      - 2
      - 0
    .max_flat_workgroup_size: 512
    .name:           _Z7k_frontPKfPmS0_S0_S0_S0_S0_S0_PDF16_S2_PfS3_S0_S2_S0_S2_S3_S3_S3_
    .private_segment_fixed_size: 0
    .sgpr_count:     88
    .sgpr_spill_count: 0
    .symbol:         _Z7k_frontPKfPmS0_S0_S0_S0_S0_S0_PDF16_S2_PfS3_S0_S2_S0_S2_S3_S3_S3_.kd
    .uniform_work_group_size: 1
    .uses_dynamic_stack: false
    .vgpr_count:     68
    .vgpr_spill_count: 0
    .wavefront_size: 64
  - .agpr_count:     256
    .args:
      - .actual_access:  read_only
        .address_space:  global
        .offset:         0
        .size:           8
        .value_kind:     global_buffer
      - .actual_access:  read_only
        .address_space:  global
        .offset:         8
        .size:           8
        .value_kind:     global_buffer
      - .actual_access:  read_only
        .address_space:  global
        .offset:         16
        .size:           8
        .value_kind:     global_buffer
      - .actual_access:  read_only
        .address_space:  global
        .offset:         24
        .size:           8
        .value_kind:     global_buffer
      - .actual_access:  read_only
        .address_space:  global
        .offset:         32
        .size:           8
        .value_kind:     global_buffer
      - .address_space:  global
        .offset:         40
        .size:           8
        .value_kind:     global_buffer
      - .actual_access:  write_only
        .address_space:  global
        .offset:         48
        .size:           8
        .value_kind:     global_buffer
      - .actual_access:  write_only
        .address_space:  global
        .offset:         56
        .size:           8
        .value_kind:     global_buffer
    .group_segment_fixed_size: 114688
    .kernarg_segment_align: 8
    .kernarg_segment_size: 64
    .language:       OpenCL C
    .language_version:
      - 2
      - 0
    .max_flat_workgroup_size: 256
    .name:           _Z6k_mainPKDF16_PKfS2_S2_PKmPjPfS6_
    .private_segment_fixed_size: 0
    .sgpr_count:     108
    .sgpr_spill_count: 0
    .symbol:         _Z6k_mainPKDF16_PKfS2_S2_PKmPjPfS6_.kd
    .uniform_work_group_size: 1
    .uses_dynamic_stack: false
    .vgpr_count:     492
    .vgpr_spill_count: 0
    .wavefront_size: 64
  - .agpr_count:     0
    .args:
      - .actual_access:  read_only
        .address_space:  global
        .offset:         0
        .size:           8
        .value_kind:     global_buffer
      - .actual_access:  read_only
        .address_space:  global
        .offset:         8
        .size:           8
        .value_kind:     global_buffer
      - .actual_access:  read_only
        .address_space:  global
        .offset:         16
        .size:           8
        .value_kind:     global_buffer
      - .actual_access:  read_only
        .address_space:  global
        .offset:         24
        .size:           8
        .value_kind:     global_buffer
      - .actual_access:  read_only
        .address_space:  global
        .offset:         32
        .size:           8
        .value_kind:     global_buffer
      - .actual_access:  read_only
        .address_space:  global
        .offset:         40
        .size:           8
        .value_kind:     global_buffer
      - .actual_access:  read_only
        .address_space:  global
        .offset:         48
        .size:           8
        .value_kind:     global_buffer
      - .actual_access:  read_only
        .address_space:  global
        .offset:         56
        .size:           8
        .value_kind:     global_buffer
      - .actual_access:  read_only
        .address_space:  global
        .offset:         64
        .size:           8
        .value_kind:     global_buffer
      - .actual_access:  write_only
        .address_space:  global
        .offset:         72
        .size:           8
        .value_kind:     global_buffer
      - .actual_access:  write_only
        .address_space:  global
        .offset:         80
        .size:           8
        .value_kind:     global_buffer
    .group_segment_fixed_size: 101632
    .kernarg_segment_align: 8
    .kernarg_segment_size: 88
    .language:       OpenCL C
    .language_version:
      - 2
      - 0
    .max_flat_workgroup_size: 256
    .name:           _Z7k_graphPKfS0_S0_S0_S0_S0_S0_S0_S0_PfS1_
    .private_segment_fixed_size: 0
    .sgpr_count:     25
    .sgpr_spill_count: 0
    .symbol:         _Z7k_graphPKfS0_S0_S0_S0_S0_S0_S0_S0_PfS1_.kd
    .uniform_work_group_size: 1
    .uses_dynamic_stack: false
    .vgpr_count:     236
    .vgpr_spill_count: 0
    .wavefront_size: 64
  - .agpr_count:     0
    .args:
      - .actual_access:  read_only
        .address_space:  global
        .offset:         0
        .size:           8
        .value_kind:     global_buffer
      - .actual_access:  read_only
        .address_space:  global
        .offset:         8
        .size:           8
        .value_kind:     global_buffer
      - .actual_access:  read_only
        .address_space:  global
        .offset:         16
        .size:           8
        .value_kind:     global_buffer
      - .actual_access:  read_only
        .address_space:  global
        .offset:         24
        .size:           8
        .value_kind:     global_buffer
      - .actual_access:  read_only
        .address_space:  global
        .offset:         32
        .size:           8
        .value_kind:     global_buffer
      - .actual_access:  read_only
        .address_space:  global
        .offset:         40
        .size:           8
        .value_kind:     global_buffer
      - .actual_access:  read_only
        .address_space:  global
        .offset:         48
        .size:           8
        .value_kind:     global_buffer
      - .address_space:  global
        .offset:         56
        .size:           8
        .value_kind:     global_buffer
      - .actual_access:  read_only
        .address_space:  global
        .offset:         64
        .size:           8
        .value_kind:     global_buffer
      - .actual_access:  read_only
        .address_space:  global
        .offset:         72
        .size:           8
        .value_kind:     global_buffer
      - .actual_access:  read_only
        .address_space:  global
        .offset:         80
        .size:           8
        .value_kind:     global_buffer
      - .address_space:  global
        .offset:         88
        .size:           8
        .value_kind:     global_buffer
      - .actual_access:  write_only
        .address_space:  global
        .offset:         96
        .size:           8
        .value_kind:     global_buffer
      - .actual_access:  write_only
        .address_space:  global
        .offset:         104
        .size:           8
        .value_kind:     global_buffer
      - .actual_access:  write_only
        .address_space:  global
        .offset:         112
        .size:           8
        .value_kind:     global_buffer
      - .actual_access:  read_only
        .address_space:  global
        .offset:         120
        .size:           8
        .value_kind:     global_buffer
      - .actual_access:  read_only
        .address_space:  global
        .offset:         128
        .size:           8
        .value_kind:     global_buffer
      - .actual_access:  read_only
        .address_space:  global
        .offset:         136
        .size:           8
        .value_kind:     global_buffer
      - .actual_access:  read_only
        .address_space:  global
        .offset:         144
        .size:           8
        .value_kind:     global_buffer
      - .actual_access:  read_only
        .address_space:  global
        .offset:         152
        .size:           8
        .value_kind:     global_buffer
      - .actual_access:  read_only
        .address_space:  global
        .offset:         160
        .size:           8
        .value_kind:     global_buffer
      - .actual_access:  read_only
        .address_space:  global
        .offset:         168
        .size:           8
        .value_kind:     global_buffer
    .group_segment_fixed_size: 53792
    .kernarg_segment_align: 8
    .kernarg_segment_size: 176
    .language:       OpenCL C
    .language_version:
      - 2
      - 0
    .max_flat_workgroup_size: 512
    .name:           _Z9k_redprepILi1EEvPKfPKjS1_S1_S1_S1_S1_PfPKDv8_DF16_S7_S1_PDF16_S4_S4_S4_PKiS7_S1_S1_S1_S4_S4_
    .private_segment_fixed_size: 0
    .sgpr_count:     106
    .sgpr_spill_count: 4
    .symbol:         _Z9k_redprepILi1EEvPKfPKjS1_S1_S1_S1_S1_PfPKDv8_DF16_S7_S1_PDF16_S4_S4_S4_PKiS7_S1_S1_S1_S4_S4_.kd
    .uniform_work_group_size: 1
    .uses_dynamic_stack: false
    .vgpr_count:     104
    .vgpr_spill_count: 0
    .wavefront_size: 64
  - .agpr_count:     0
    .args:
      - .actual_access:  read_only
        .address_space:  global
        .offset:         0
        .size:           8
        .value_kind:     global_buffer
      - .actual_access:  read_only
        .address_space:  global
        .offset:         8
        .size:           8
        .value_kind:     global_buffer
      - .actual_access:  read_only
        .address_space:  global
        .offset:         16
        .size:           8
        .value_kind:     global_buffer
      - .actual_access:  read_only
        .address_space:  global
        .offset:         24
        .size:           8
        .value_kind:     global_buffer
      - .actual_access:  read_only
        .address_space:  global
        .offset:         32
        .size:           8
        .value_kind:     global_buffer
      - .actual_access:  read_only
        .address_space:  global
        .offset:         40
        .size:           8
        .value_kind:     global_buffer
      - .actual_access:  read_only
        .address_space:  global
        .offset:         48
        .size:           8
        .value_kind:     global_buffer
      - .address_space:  global
        .offset:         56
        .size:           8
        .value_kind:     global_buffer
      - .actual_access:  read_only
        .address_space:  global
        .offset:         64
        .size:           8
        .value_kind:     global_buffer
      - .actual_access:  read_only
        .address_space:  global
        .offset:         72
        .size:           8
        .value_kind:     global_buffer
      - .actual_access:  read_only
        .address_space:  global
        .offset:         80
        .size:           8
        .value_kind:     global_buffer
      - .actual_access:  read_only
        .address_space:  global
        .offset:         88
        .size:           8
        .value_kind:     global_buffer
      - .actual_access:  read_only
        .address_space:  global
        .offset:         96
        .size:           8
        .value_kind:     global_buffer
      - .actual_access:  read_only
        .address_space:  global
        .offset:         104
        .size:           8
        .value_kind:     global_buffer
      - .actual_access:  read_only
        .address_space:  global
        .offset:         112
        .size:           8
        .value_kind:     global_buffer
      - .actual_access:  read_only
        .address_space:  global
        .offset:         120
        .size:           8
        .value_kind:     global_buffer
      - .actual_access:  read_only
        .address_space:  global
        .offset:         128
        .size:           8
        .value_kind:     global_buffer
      - .actual_access:  read_only
        .address_space:  global
        .offset:         136
        .size:           8
        .value_kind:     global_buffer
      - .actual_access:  read_only
        .address_space:  global
        .offset:         144
        .size:           8
        .value_kind:     global_buffer
      - .actual_access:  read_only
        .address_space:  global
        .offset:         152
        .size:           8
        .value_kind:     global_buffer
      - .actual_access:  write_only
        .address_space:  global
        .offset:         160
        .size:           8
        .value_kind:     global_buffer
      - .address_space:  global
        .offset:         168
        .size:           8
        .value_kind:     global_buffer
    .group_segment_fixed_size: 66688
    .kernarg_segment_align: 8
    .kernarg_segment_size: 176
    .language:       OpenCL C
    .language_version:
      - 2
      - 0
    .max_flat_workgroup_size: 512
    .name:           _Z9k_redprepILi2EEvPKfPKjS1_S1_S1_S1_S1_PfPKDv8_DF16_S7_S1_PDF16_S4_S4_S4_PKiS7_S1_S1_S1_S4_S4_
    .private_segment_fixed_size: 0
    .sgpr_count:     102
    .sgpr_spill_count: 0
    .symbol:         _Z9k_redprepILi2EEvPKfPKjS1_S1_S1_S1_S1_PfPKDv8_DF16_S7_S1_PDF16_S4_S4_S4_PKiS7_S1_S1_S1_S4_S4_.kd
    .uniform_work_group_size: 1
    .uses_dynamic_stack: false
    .vgpr_count:     106
    .vgpr_spill_count: 0
    .wavefront_size: 64
